# SWAP,16 reduction step via v_permlane16_swap instead of ds_swizzle (11 sites), on top of the DPP reductions
# baseline (speedup 1.0000x reference)
.LBB0_140:
	v_cvt_pk_f32_fp8_sdwa v[52:53], v100 src0_sel:WORD_1
	v_cvt_pk_f32_fp8_e32 v[54:55], v100
	v_cvt_pk_f32_fp8_sdwa v[102:103], v101 src0_sel:WORD_1
	v_cvt_pk_f32_fp8_e32 v[104:105], v98
	v_cvt_pk_f32_fp8_sdwa v[106:107], v98 src0_sel:WORD_1
	v_cvt_pk_f32_fp8_e32 v[108:109], v99
	v_cvt_pk_f32_fp8_sdwa v[98:99], v99 src0_sel:WORD_1
	v_cvt_pk_f32_fp8_e32 v[100:101], v101
	v_pk_add_f32 v[52:53], v[52:53], 0 op_sel_hi:[1,0]
	v_pk_add_f32 v[54:55], v[54:55], 0 op_sel_hi:[1,0]
	v_pk_add_f32 v[102:103], v[102:103], 0 op_sel_hi:[1,0]
	v_pk_add_f32 v[54:55], v[54:55], v[104:105]
	v_pk_add_f32 v[52:53], v[52:53], v[106:107]
	v_pk_add_f32 v[98:99], v[102:103], v[98:99]
	v_cvt_pk_f32_fp8_sdwa v[102:103], v96 src0_sel:WORD_1
	v_cvt_pk_f32_fp8_e32 v[104:105], v96
	v_cvt_pk_f32_fp8_sdwa v[106:107], v97 src0_sel:WORD_1
	v_cvt_pk_f32_fp8_e32 v[96:97], v97
	v_pk_add_f32 v[100:101], v[100:101], 0 op_sel_hi:[1,0]
	v_pk_add_f32 v[52:53], v[52:53], v[102:103]
	v_pk_add_f32 v[100:101], v[100:101], v[108:109]
	v_pk_add_f32 v[54:55], v[54:55], v[104:105]
	v_pk_add_f32 v[96:97], v[100:101], v[96:97]
	v_cvt_pk_f32_fp8_e32 v[100:101], v94
	v_cvt_pk_f32_fp8_sdwa v[102:103], v94 src0_sel:WORD_1
	v_cvt_pk_f32_fp8_e32 v[104:105], v95
	v_cvt_pk_f32_fp8_sdwa v[94:95], v95 src0_sel:WORD_1
	v_pk_add_f32 v[98:99], v[98:99], v[106:107]
	v_pk_add_f32 v[54:55], v[54:55], v[100:101]
	v_pk_add_f32 v[52:53], v[52:53], v[102:103]
	v_pk_add_f32 v[96:97], v[96:97], v[104:105]
	v_pk_add_f32 v[94:95], v[98:99], v[94:95]
	v_lshlrev_b32_e32 v98, 16, v36
	v_and_b32_e32 v99, 0xffff0000, v36
	v_lshlrev_b32_e32 v36, 16, v37
	v_and_b32_e32 v37, 0xffff0000, v37
	v_lshlrev_b32_e32 v100, 16, v38
	v_and_b32_e32 v101, 0xffff0000, v38
	v_lshlrev_b32_e32 v38, 16, v39
	v_and_b32_e32 v39, 0xffff0000, v39
	v_pk_fma_f32 v[36:37], v[2:3], v[52:53], v[36:37]
	v_pk_fma_f32 v[52:53], v[0:1], v[54:55], v[98:99]
	v_pk_fma_f32 v[38:39], v[6:7], v[94:95], v[38:39]
	v_pk_fma_f32 v[54:55], v[4:5], v[96:97], v[100:101]
	v_cvt_pk_f32_fp8_sdwa v[94:95], v92 src0_sel:WORD_1
	v_cvt_pk_f32_fp8_e32 v[96:97], v92
	v_cvt_pk_f32_fp8_sdwa v[98:99], v93 src0_sel:WORD_1
	v_cvt_pk_f32_fp8_e32 v[100:101], v86
	v_cvt_pk_f32_fp8_sdwa v[102:103], v86 src0_sel:WORD_1
	v_cvt_pk_f32_fp8_e32 v[104:105], v87
	v_cvt_pk_f32_fp8_sdwa v[86:87], v87 src0_sel:WORD_1
	v_cvt_pk_f32_fp8_e32 v[92:93], v93
	v_pk_add_f32 v[94:95], v[94:95], 0 op_sel_hi:[1,0]
	v_pk_add_f32 v[96:97], v[96:97], 0 op_sel_hi:[1,0]
	v_pk_add_f32 v[98:99], v[98:99], 0 op_sel_hi:[1,0]
	v_pk_add_f32 v[96:97], v[96:97], v[100:101]
	v_pk_add_f32 v[94:95], v[94:95], v[102:103]
	v_pk_add_f32 v[86:87], v[98:99], v[86:87]
	v_cvt_pk_f32_fp8_sdwa v[98:99], v58 src0_sel:WORD_1
	v_cvt_pk_f32_fp8_e32 v[100:101], v58
	v_cvt_pk_f32_fp8_sdwa v[102:103], v59 src0_sel:WORD_1
	v_cvt_pk_f32_fp8_e32 v[58:59], v59
	v_pk_add_f32 v[92:93], v[92:93], 0 op_sel_hi:[1,0]
	v_pk_add_f32 v[94:95], v[94:95], v[98:99]
	v_pk_add_f32 v[92:93], v[92:93], v[104:105]
	v_pk_add_f32 v[96:97], v[96:97], v[100:101]
	v_pk_add_f32 v[58:59], v[92:93], v[58:59]
	v_cvt_pk_f32_fp8_e32 v[92:93], v56
	v_cvt_pk_f32_fp8_sdwa v[98:99], v56 src0_sel:WORD_1
	v_cvt_pk_f32_fp8_e32 v[100:101], v57
	v_cvt_pk_f32_fp8_sdwa v[56:57], v57 src0_sel:WORD_1
	v_pk_add_f32 v[86:87], v[86:87], v[102:103]
	v_pk_add_f32 v[94:95], v[94:95], v[98:99]
	v_pk_add_f32 v[92:93], v[96:97], v[92:93]
	v_pk_add_f32 v[56:57], v[86:87], v[56:57]
	v_lshlrev_b32_e32 v86, 16, v32
	v_and_b32_e32 v87, 0xffff0000, v32
	v_lshlrev_b32_e32 v32, 16, v33
	v_and_b32_e32 v33, 0xffff0000, v33
	v_pk_fma_f32 v[94:95], v[18:19], v[94:95], v[32:33]
	v_mul_f32_e32 v32, v53, v53
	v_mul_f32_e32 v33, v37, v37
	v_lshlrev_b32_e32 v96, 16, v34
	v_and_b32_e32 v97, 0xffff0000, v34
	v_lshlrev_b32_e32 v34, 16, v35
	v_and_b32_e32 v35, 0xffff0000, v35
	v_fmac_f32_e32 v32, v52, v52
	v_fmac_f32_e32 v33, v36, v36
	v_pk_fma_f32 v[56:57], v[22:23], v[56:57], v[34:35]
	v_add_f32_e32 v32, v32, v33
	v_mul_f32_e32 v33, v55, v55
	v_mul_f32_e32 v34, v39, v39
	v_fmac_f32_e32 v33, v54, v54
	v_fmac_f32_e32 v34, v38, v38
	v_pk_fma_f32 v[86:87], v[16:17], v[92:93], v[86:87]
	v_add_f32_e32 v33, v33, v34
	v_add_f32_e32 v32, v32, v33
	v_mul_f32_e32 v33, v87, v87
	v_mul_f32_e32 v34, v95, v95
	v_pk_add_f32 v[58:59], v[58:59], v[100:101]
	v_fmac_f32_e32 v33, v86, v86
	v_fmac_f32_e32 v34, v94, v94
	v_pk_fma_f32 v[58:59], v[20:21], v[58:59], v[96:97]
	v_add_f32_e32 v33, v33, v34
	v_add_f32_e32 v32, v32, v33
	v_mul_f32_e32 v33, v59, v59
	v_mul_f32_e32 v34, v57, v57
	v_fmac_f32_e32 v33, v58, v58
	v_fmac_f32_e32 v34, v56, v56
	v_add_f32_e32 v33, v33, v34
	v_add_f32_e32 v32, v32, v33
	s_nop 1
	v_mov_b32_dpp v33, v32 quad_perm:[1,0,3,2] row_mask:0xf bank_mask:0xf
	s_mov_b64 s[14:15], 0xed40800
	v_lshl_add_u64 v[92:93], v[72:73], 0, s[14:15]
	v_cvt_pk_bf16_f32 v34, v54, v55
	s_mov_b64 s[14:15], 0xed40c00
	s_waitcnt lgkmcnt(0)
	v_add_f32_e32 v32, v32, v33
	s_nop 1
	v_mov_b32_dpp v33, v32 quad_perm:[2,3,0,1] row_mask:0xf bank_mask:0xf
	v_lshl_add_u64 v[72:73], v[72:73], 0, s[14:15]
	v_lshl_add_u64 v[66:67], v[66:67], 0, s[80:81]
	v_lshl_add_u64 v[68:69], v[68:69], 0, s[84:85]
	s_mov_b32 s14, s7
	s_waitcnt lgkmcnt(0)
	v_add_f32_e32 v32, v32, v33
	s_nop 1
	v_mov_b32_dpp v33, v32 row_half_mirror row_mask:0xf bank_mask:0xf
	s_waitcnt lgkmcnt(0)
	v_add_f32_e32 v35, v32, v33
	s_nop 1
	v_mov_b32_dpp v96, v35 row_mirror row_mask:0xf bank_mask:0xf
	v_cvt_pk_bf16_f32 v32, v52, v53
	v_cvt_pk_bf16_f32 v33, v36, v37
	s_waitcnt lgkmcnt(0)
	v_add_f32_e32 v96, v35, v96
	v_mov_b32_e32 v97, v96
	s_nop 1
	v_permlane16_swap_b32_e32 v96, v97
	v_cvt_pk_bf16_f32 v35, v38, v39
	global_store_dwordx4 v[92:93], v[32:35], off
	s_waitcnt lgkmcnt(0)
	s_nop 0
	v_add_f32_e32 v34, v96, v97
	v_mov_b32_e32 v35, v34
	s_nop 1
	v_permlane32_swap_b32_e32 v34, v35
	v_add_f32_e32 v34, v34, v35
	v_fmamk_f32 v34, v34, 0x3a800000, v196
	v_mul_f32_e32 v35, 0x4b800000, v34
	v_cmp_gt_f32_e32 vcc, s35, v34
	v_cvt_pk_bf16_f32 v32, v86, v87
	v_cvt_pk_bf16_f32 v33, v94, v95
	v_cndmask_b32_e32 v34, v34, v35, vcc
	v_rsq_f32_e32 v92, v34
	v_cvt_pk_bf16_f32 v34, v58, v59
	v_cvt_pk_bf16_f32 v35, v56, v57
	global_store_dwordx4 v[72:73], v[32:35], off
	s_nop 1
	v_mul_f32_e32 v32, 0x45800000, v92
	v_cndmask_b32_e32 v72, v92, v32, vcc
	v_pk_mul_f32 v[32:33], v[52:53], v[72:73] op_sel_hi:[1,0]
	v_pk_mul_f32 v[34:35], v[36:37], v[72:73] op_sel_hi:[1,0]
	v_pk_mul_f32 v[36:37], v[54:55], v[72:73] op_sel_hi:[1,0]
	v_pk_fma_f32 v[32:33], v[74:75], v[32:33], v[28:29]
	v_pk_fma_f32 v[36:37], v[80:81], v[36:37], v[24:25]
	v_mov_b32_e32 v52, v113
	v_mov_b32_e32 v53, v113
	v_cvt_pk_fp8_f32 v52, v32, v33
	v_cvt_pk_fp8_f32 v53, v36, v37
	v_pk_mul_f32 v[38:39], v[38:39], v[72:73] op_sel_hi:[1,0]
	v_pk_fma_f32 v[34:35], v[76:77], v[34:35], v[30:31]
	v_pk_fma_f32 v[38:39], v[78:79], v[38:39], v[26:27]
	v_cvt_pk_fp8_f32 v52, v34, v35 op_sel:[0,0,1]
	v_cvt_pk_fp8_f32 v53, v38, v39 op_sel:[0,0,1]
	v_cvt_pk_bf16_f32 v32, v32, v33
	v_cvt_pk_bf16_f32 v33, v34, v35
	v_cvt_pk_bf16_f32 v34, v36, v37
	v_cvt_pk_bf16_f32 v35, v38, v39
	global_store_dwordx4 v[48:49], v[32:35], off offset:2048
	global_store_dwordx2 v[50:51], v[52:53], off offset:1024
	v_pk_mul_f32 v[36:37], v[58:59], v[72:73] op_sel_hi:[1,0]
	v_pk_mul_f32 v[32:33], v[86:87], v[72:73] op_sel_hi:[1,0]
	s_waitcnt vmcnt(5)
	v_pk_fma_f32 v[36:37], v[90:91], v[36:37], v[40:41]
	s_waitcnt vmcnt(4)
	v_pk_fma_f32 v[32:33], v[84:85], v[32:33], v[44:45]
	v_mov_b32_e32 v52, v113
	v_mov_b32_e32 v53, v113
	v_cvt_pk_fp8_f32 v52, v32, v33
	v_cvt_pk_fp8_f32 v53, v36, v37
	v_pk_mul_f32 v[34:35], v[94:95], v[72:73] op_sel_hi:[1,0]
	v_pk_mul_f32 v[38:39], v[56:57], v[72:73] op_sel_hi:[1,0]
	v_pk_fma_f32 v[34:35], v[82:83], v[34:35], v[46:47]
	v_pk_fma_f32 v[38:39], v[88:89], v[38:39], v[42:43]
	v_cvt_pk_fp8_f32 v52, v34, v35 op_sel:[0,0,1]
	v_cvt_pk_fp8_f32 v53, v38, v39 op_sel:[0,0,1]
	v_cvt_pk_bf16_f32 v32, v32, v33
	v_cvt_pk_bf16_f32 v33, v34, v35
	v_cvt_pk_bf16_f32 v34, v36, v37
	v_cvt_pk_bf16_f32 v35, v38, v39
	global_store_dwordx4 v[48:49], v[32:35], off offset:3072
	global_store_dwordx2 v[50:51], v[52:53], off offset:1536
	v_mov_b64_e32 v[58:59], v[10:11]
	v_mov_b64_e32 v[34:35], v[14:15]
	s_andn2_b64 vcc, exec, s[38:39]
	v_mov_b64_e32 v[32:33], v[12:13]
	v_mov_b64_e32 v[56:57], v[8:9]
	s_cbranch_vccz .LBB0_145

.LBB0_143:
	s_waitcnt vmcnt(17)
	v_cvt_pk_f32_fp8_sdwa v[120:121], v118 src0_sel:WORD_1
	v_cvt_pk_f32_fp8_e32 v[122:123], v118
	v_cvt_pk_f32_fp8_sdwa v[124:125], v119 src0_sel:WORD_1
	s_waitcnt vmcnt(16)
	v_cvt_pk_f32_fp8_e32 v[126:127], v116
	v_cvt_pk_f32_fp8_sdwa v[128:129], v116 src0_sel:WORD_1
	v_cvt_pk_f32_fp8_e32 v[130:131], v117
	v_cvt_pk_f32_fp8_sdwa v[116:117], v117 src0_sel:WORD_1
	v_cvt_pk_f32_fp8_e32 v[118:119], v119
	v_pk_add_f32 v[120:121], v[120:121], 0 op_sel_hi:[1,0]
	v_pk_add_f32 v[122:123], v[122:123], 0 op_sel_hi:[1,0]
	v_pk_add_f32 v[124:125], v[124:125], 0 op_sel_hi:[1,0]
	v_pk_add_f32 v[122:123], v[122:123], v[126:127]
	v_pk_add_f32 v[120:121], v[120:121], v[128:129]
	v_pk_add_f32 v[116:117], v[124:125], v[116:117]
	s_waitcnt vmcnt(13)
	v_cvt_pk_f32_fp8_sdwa v[124:125], v114 src0_sel:WORD_1
	v_cvt_pk_f32_fp8_e32 v[126:127], v114
	v_cvt_pk_f32_fp8_sdwa v[128:129], v115 src0_sel:WORD_1
	v_cvt_pk_f32_fp8_e32 v[114:115], v115
	v_pk_add_f32 v[118:119], v[118:119], 0 op_sel_hi:[1,0]
	v_pk_add_f32 v[120:121], v[120:121], v[124:125]
	v_pk_add_f32 v[118:119], v[118:119], v[130:131]
	v_pk_add_f32 v[122:123], v[122:123], v[126:127]
	v_pk_add_f32 v[114:115], v[118:119], v[114:115]
	s_waitcnt vmcnt(12)
	v_cvt_pk_f32_fp8_e32 v[118:119], v110
	v_cvt_pk_f32_fp8_sdwa v[124:125], v110 src0_sel:WORD_1
	v_cvt_pk_f32_fp8_e32 v[126:127], v111
	v_cvt_pk_f32_fp8_sdwa v[110:111], v111 src0_sel:WORD_1
	v_pk_add_f32 v[116:117], v[116:117], v[128:129]
	v_pk_add_f32 v[118:119], v[122:123], v[118:119]
	v_pk_add_f32 v[120:121], v[120:121], v[124:125]
	v_pk_add_f32 v[114:115], v[114:115], v[126:127]
	v_pk_add_f32 v[110:111], v[116:117], v[110:111]
	v_lshlrev_b32_e32 v116, 16, v52
	v_and_b32_e32 v117, 0xffff0000, v52
	v_lshlrev_b32_e32 v52, 16, v53
	v_and_b32_e32 v53, 0xffff0000, v53
	v_lshlrev_b32_e32 v122, 16, v54
	v_and_b32_e32 v123, 0xffff0000, v54
	v_lshlrev_b32_e32 v54, 16, v55
	v_and_b32_e32 v55, 0xffff0000, v55
	v_pk_fma_f32 v[52:53], v[2:3], v[120:121], v[52:53]
	v_pk_fma_f32 v[116:117], v[0:1], v[118:119], v[116:117]
	v_pk_fma_f32 v[54:55], v[6:7], v[110:111], v[54:55]
	v_pk_fma_f32 v[110:111], v[4:5], v[114:115], v[122:123]
	v_cvt_pk_f32_fp8_sdwa v[114:115], v108 src0_sel:WORD_1
	v_cvt_pk_f32_fp8_e32 v[118:119], v108
	v_cvt_pk_f32_fp8_sdwa v[120:121], v109 src0_sel:WORD_1
	v_cvt_pk_f32_fp8_e32 v[122:123], v106
	v_cvt_pk_f32_fp8_sdwa v[124:125], v106 src0_sel:WORD_1
	v_cvt_pk_f32_fp8_e32 v[126:127], v107
	v_cvt_pk_f32_fp8_sdwa v[106:107], v107 src0_sel:WORD_1
	v_cvt_pk_f32_fp8_e32 v[108:109], v109
	v_pk_add_f32 v[114:115], v[114:115], 0 op_sel_hi:[1,0]
	v_pk_add_f32 v[118:119], v[118:119], 0 op_sel_hi:[1,0]
	v_pk_add_f32 v[120:121], v[120:121], 0 op_sel_hi:[1,0]
	v_pk_add_f32 v[118:119], v[118:119], v[122:123]
	v_pk_add_f32 v[114:115], v[114:115], v[124:125]
	v_pk_add_f32 v[106:107], v[120:121], v[106:107]
	s_waitcnt vmcnt(10)
	v_cvt_pk_f32_fp8_sdwa v[120:121], v104 src0_sel:WORD_1
	v_cvt_pk_f32_fp8_e32 v[122:123], v104
	v_cvt_pk_f32_fp8_sdwa v[124:125], v105 src0_sel:WORD_1
	v_cvt_pk_f32_fp8_e32 v[104:105], v105
	v_pk_add_f32 v[108:109], v[108:109], 0 op_sel_hi:[1,0]
	v_pk_add_f32 v[114:115], v[114:115], v[120:121]
	v_pk_add_f32 v[108:109], v[108:109], v[126:127]
	v_pk_add_f32 v[118:119], v[118:119], v[122:123]
	v_pk_add_f32 v[104:105], v[108:109], v[104:105]
	v_cvt_pk_f32_fp8_e32 v[108:109], v102
	v_cvt_pk_f32_fp8_sdwa v[120:121], v102 src0_sel:WORD_1
	v_cvt_pk_f32_fp8_e32 v[122:123], v103
	v_cvt_pk_f32_fp8_sdwa v[102:103], v103 src0_sel:WORD_1
	v_pk_add_f32 v[106:107], v[106:107], v[124:125]
	v_pk_add_f32 v[114:115], v[114:115], v[120:121]
	v_pk_add_f32 v[108:109], v[118:119], v[108:109]
	v_pk_add_f32 v[102:103], v[106:107], v[102:103]
	v_lshlrev_b32_e32 v106, 16, v48
	v_and_b32_e32 v107, 0xffff0000, v48
	v_lshlrev_b32_e32 v48, 16, v49
	v_and_b32_e32 v49, 0xffff0000, v49
	v_pk_fma_f32 v[114:115], v[18:19], v[114:115], v[48:49]
	v_mul_f32_e32 v48, v117, v117
	v_mul_f32_e32 v49, v53, v53
	v_lshlrev_b32_e32 v118, 16, v50
	v_and_b32_e32 v119, 0xffff0000, v50
	v_lshlrev_b32_e32 v50, 16, v51
	v_and_b32_e32 v51, 0xffff0000, v51
	v_fmac_f32_e32 v48, v116, v116
	v_fmac_f32_e32 v49, v52, v52
	v_pk_fma_f32 v[102:103], v[22:23], v[102:103], v[50:51]
	v_add_f32_e32 v48, v48, v49
	v_mul_f32_e32 v49, v111, v111
	v_mul_f32_e32 v50, v55, v55
	v_fmac_f32_e32 v49, v110, v110
	v_fmac_f32_e32 v50, v54, v54
	v_pk_fma_f32 v[106:107], v[16:17], v[108:109], v[106:107]
	v_add_f32_e32 v49, v49, v50
	v_add_f32_e32 v48, v48, v49
	v_mul_f32_e32 v49, v107, v107
	v_mul_f32_e32 v50, v115, v115
	v_pk_add_f32 v[104:105], v[104:105], v[122:123]
	v_fmac_f32_e32 v49, v106, v106
	v_fmac_f32_e32 v50, v114, v114
	v_pk_fma_f32 v[104:105], v[20:21], v[104:105], v[118:119]
	v_add_f32_e32 v49, v49, v50
	v_add_f32_e32 v48, v48, v49
	v_mul_f32_e32 v49, v105, v105
	v_mul_f32_e32 v50, v103, v103
	v_fmac_f32_e32 v49, v104, v104
	v_fmac_f32_e32 v50, v102, v102
	v_add_f32_e32 v49, v49, v50
	v_add_f32_e32 v48, v48, v49
	s_nop 1
	v_mov_b32_dpp v49, v48 quad_perm:[1,0,3,2] row_mask:0xf bank_mask:0xf
	s_mov_b64 s[26:27], 0xed40000
	v_lshl_add_u64 v[108:109], v[72:73], 0, s[26:27]
	v_cvt_pk_bf16_f32 v50, v110, v111
	s_mov_b64 s[26:27], 0xed40400
	s_waitcnt lgkmcnt(0)
	v_add_f32_e32 v48, v48, v49
	s_nop 1
	v_mov_b32_dpp v49, v48 quad_perm:[2,3,0,1] row_mask:0xf bank_mask:0xf
	s_mov_b32 s15, s13
	v_lshl_add_u64 v[118:119], v[72:73], 0, s[26:27]
	s_add_i32 s13, s14, 1
	s_mul_hi_i32 s14, s13, 0x78787879
	s_waitcnt lgkmcnt(0)
	v_add_f32_e32 v48, v48, v49
	s_nop 1
	v_mov_b32_dpp v49, v48 row_half_mirror row_mask:0xf bank_mask:0xf
	s_lshr_b32 s25, s14, 31
	s_ashr_i32 s14, s14, 11
	s_add_i32 s14, s14, s25
	s_mul_i32 s25, s14, 0xffffef00
	s_waitcnt lgkmcnt(0)
	v_add_f32_e32 v51, v48, v49
	s_nop 1
	v_mov_b32_dpp v112, v51 row_mirror row_mask:0xf bank_mask:0xf
	v_cvt_pk_bf16_f32 v48, v116, v117
	v_cvt_pk_bf16_f32 v49, v52, v53
	s_add_i32 s13, s13, s25
	s_cmpk_gt_i32 s13, 0xff
	s_waitcnt lgkmcnt(0)
	v_add_f32_e32 v112, v51, v112
	v_mov_b32_e32 v120, v112
	s_nop 1
	v_permlane16_swap_b32_e32 v112, v120
	v_cvt_pk_bf16_f32 v51, v54, v55
	global_store_dwordx4 v[108:109], v[48:51], off
	s_cselect_b32 s13, s14, 16
	s_mov_b32 s14, 0x17dd9000
	s_waitcnt lgkmcnt(0)
	v_add_f32_e32 v50, v112, v120
	v_mov_b32_e32 v51, v50
	s_nop 1
	v_permlane32_swap_b32_e32 v50, v51
	v_add_f32_e32 v50, v50, v51
	v_fmamk_f32 v50, v50, 0x3a800000, v196
	v_mul_f32_e32 v51, 0x4b800000, v50
	v_cmp_gt_f32_e32 vcc, s35, v50
	v_cvt_pk_bf16_f32 v48, v106, v107
	v_cvt_pk_bf16_f32 v49, v114, v115
	v_cndmask_b32_e32 v50, v50, v51, vcc
	v_rsq_f32_e32 v108, v50
	v_cvt_pk_bf16_f32 v50, v104, v105
	v_cvt_pk_bf16_f32 v51, v102, v103
	global_store_dwordx4 v[118:119], v[48:51], off
	v_mov_b32_e32 v119, v113
	v_mov_b32_e32 v118, v113
	v_mul_f32_e32 v48, 0x45800000, v108
	v_cndmask_b32_e32 v108, v108, v48, vcc
	v_pk_mul_f32 v[50:51], v[52:53], v[108:109] op_sel_hi:[1,0]
	v_pk_mul_f32 v[48:49], v[116:117], v[108:109] op_sel_hi:[1,0]
	v_pk_fma_f32 v[116:117], v[76:77], v[50:51], v[30:31]
	v_pk_mul_f32 v[50:51], v[110:111], v[108:109] op_sel_hi:[1,0]
	v_pk_fma_f32 v[48:49], v[74:75], v[48:49], v[28:29]
	v_pk_fma_f32 v[110:111], v[80:81], v[50:51], v[24:25]
	v_pk_mul_f32 v[52:53], v[54:55], v[108:109] op_sel_hi:[1,0]
	v_cvt_pk_fp8_f32 v119, v110, v111
	v_pk_fma_f32 v[54:55], v[78:79], v[52:53], v[26:27]
	v_cvt_pk_bf16_f32 v50, v48, v49
	v_cvt_pk_fp8_f32 v118, v48, v49
	v_add_co_u32_e32 v48, vcc, s14, v72
	v_cvt_pk_bf16_f32 v51, v116, v117
	v_cvt_pk_bf16_f32 v52, v110, v111
	v_cvt_pk_bf16_f32 v53, v54, v55
	v_addc_co_u32_e32 v49, vcc, 0, v73, vcc
	global_store_dwordx4 v[48:49], v[50:53], off
	v_cvt_pk_fp8_f32 v119, v54, v55 op_sel:[0,0,1]
	v_pk_mul_f32 v[54:55], v[114:115], v[108:109] op_sel_hi:[1,0]
	v_pk_mul_f32 v[52:53], v[106:107], v[108:109] op_sel_hi:[1,0]
	s_waitcnt vmcnt(3)
	v_pk_fma_f32 v[106:107], v[82:83], v[54:55], v[46:47]
	v_pk_fma_f32 v[54:55], v[84:85], v[52:53], v[44:45]
	v_pk_mul_f32 v[52:53], v[104:105], v[108:109] op_sel_hi:[1,0]
	v_pk_mul_f32 v[102:103], v[102:103], v[108:109] op_sel_hi:[1,0]
	v_pk_fma_f32 v[104:105], v[90:91], v[52:53], v[40:41]
	v_mov_b32_e32 v108, v113
	v_mov_b32_e32 v109, v113
	v_cvt_pk_fp8_f32 v108, v54, v55
	v_cvt_pk_fp8_f32 v109, v104, v105
	v_pk_fma_f32 v[102:103], v[88:89], v[102:103], v[42:43]
	v_cvt_pk_fp8_f32 v118, v116, v117 op_sel:[0,0,1]
	v_cvt_pk_fp8_f32 v108, v106, v107 op_sel:[0,0,1]
	v_cvt_pk_fp8_f32 v109, v102, v103 op_sel:[0,0,1]
	v_lshl_add_u64 v[50:51], s[94:95], 0, v[66:67]
	s_mov_b32 s14, 0x711d9000
	v_add_co_u32_e32 v50, vcc, s14, v50
	v_cvt_pk_bf16_f32 v52, v54, v55
	s_nop 0
	v_addc_co_u32_e32 v51, vcc, 0, v51, vcc
	v_cvt_pk_bf16_f32 v53, v106, v107
	v_cvt_pk_bf16_f32 v54, v104, v105
	v_cvt_pk_bf16_f32 v55, v102, v103
	s_cmp_eq_u32 s13, s15
	global_store_dwordx2 v[50:51], v[118:119], off
	global_store_dwordx4 v[48:49], v[52:55], off offset:1024
	global_store_dwordx2 v[50:51], v[108:109], off offset:512
	s_cbranch_scc1 .LBB0_140
	s_mul_i32 s25, s13, 0x6000
	s_mul_hi_i32 s15, s13, 0x6000
	s_add_u32 s14, s60, s25
	s_addc_u32 s15, s63, s15
	v_lshl_add_u64 v[0:1], s[14:15], 0, v[70:71]
	s_mov_b64 s[14:15], 0x5000
	v_lshl_add_u64 v[16:17], v[0:1], 0, s[14:15]
	v_add_co_u32_e32 v0, vcc, 0x5000, v0
	s_mov_b32 s14, 0x3d800000
	s_nop 0
	v_addc_co_u32_e32 v1, vcc, 0, v1, vcc
	global_load_dwordx4 v[0:3], v[0:1], off
	s_nop 0
	global_load_dwordx4 v[4:7], v[16:17], off offset:16
	global_load_dwordx4 v[20:23], v[16:17], off offset:2064
	s_nop 0
	global_load_dwordx4 v[16:19], v[16:17], off offset:2048
	s_add_i32 s25, s25, 0x66000
	global_load_dwordx4 v[24:27], v[64:65], off offset:16
	global_load_dwordx4 v[28:31], v[64:65], off
	s_waitcnt vmcnt(5)
	v_pk_mul_f32 v[2:3], v[2:3], s[14:15] op_sel_hi:[1,0]
	v_pk_mul_f32 v[0:1], v[0:1], s[14:15] op_sel_hi:[1,0]
	s_waitcnt vmcnt(4)
	v_pk_mul_f32 v[6:7], v[6:7], s[14:15] op_sel_hi:[1,0]
	v_pk_mul_f32 v[4:5], v[4:5], s[14:15] op_sel_hi:[1,0]
	s_waitcnt vmcnt(2)
	v_pk_mul_f32 v[18:19], v[18:19], s[14:15] op_sel_hi:[1,0]
	v_pk_mul_f32 v[16:17], v[16:17], s[14:15] op_sel_hi:[1,0]
	v_pk_mul_f32 v[22:23], v[22:23], s[14:15] op_sel_hi:[1,0]
	v_pk_mul_f32 v[20:21], v[20:21], s[14:15] op_sel_hi:[1,0]
	s_add_i32 s14, s13, 17
	s_mul_hi_i32 s15, s14, 0x6000
	s_add_u32 s14, s60, s25
	s_addc_u32 s15, s63, s15
	v_lshl_add_u64 v[102:103], s[14:15], 0, v[70:71]
	s_movk_i32 s14, 0x1000
	v_add_co_u32_e32 v40, vcc, s14, v102
	v_lshl_add_u64 v[82:83], v[102:103], 0, s[84:85]
	s_nop 0
	v_addc_co_u32_e32 v41, vcc, 0, v103, vcc
	global_load_dwordx4 v[40:43], v[40:41], off
	s_nop 0
	global_load_dwordx4 v[44:47], v[82:83], off offset:16
	s_waitcnt vmcnt(1)
	v_pk_add_f32 v[42:43], v[42:43], 1.0 op_sel_hi:[1,0]
	v_pk_add_f32 v[40:41], v[40:41], 1.0 op_sel_hi:[1,0]
	v_pk_mul_f32 v[76:77], v[30:31], v[42:43]
	v_pk_mul_f32 v[74:75], v[28:29], v[40:41]
	s_waitcnt vmcnt(0)
	v_pk_add_f32 v[28:29], v[46:47], 1.0 op_sel_hi:[1,0]
	v_pk_add_f32 v[30:31], v[44:45], 1.0 op_sel_hi:[1,0]
	v_pk_mul_f32 v[78:79], v[26:27], v[28:29]
	v_pk_mul_f32 v[80:81], v[24:25], v[30:31]
	global_load_dwordx4 v[24:27], v[102:103], off offset:16
	global_load_dwordx4 v[28:31], v[102:103], off
	global_load_dwordx4 v[40:43], v[64:65], off offset:2064
	global_load_dwordx4 v[44:47], v[64:65], off offset:2048
	global_load_dwordx4 v[52:55], v[82:83], off offset:2064
	s_nop 0
	global_load_dwordx4 v[82:85], v[82:83], off offset:2048
	s_waitcnt vmcnt(0)
	v_pk_add_f32 v[84:85], v[84:85], 1.0 op_sel_hi:[1,0]
	v_pk_add_f32 v[88:89], v[82:83], 1.0 op_sel_hi:[1,0]
	v_pk_mul_f32 v[82:83], v[46:47], v[84:85]
	v_pk_mul_f32 v[84:85], v[44:45], v[88:89]
	v_pk_add_f32 v[44:45], v[54:55], 1.0 op_sel_hi:[1,0]
	v_pk_add_f32 v[46:47], v[52:53], 1.0 op_sel_hi:[1,0]
	v_pk_mul_f32 v[88:89], v[42:43], v[44:45]
	v_pk_mul_f32 v[90:91], v[40:41], v[46:47]
	global_load_dwordx4 v[40:43], v[102:103], off offset:2064
	global_load_dwordx4 v[44:47], v[102:103], off offset:2048
	s_branch .LBB0_140

.LBB0_148:
	v_mul_f32_e32 v32, v21, v21
	v_mul_f32_e32 v33, v23, v23
	v_fmac_f32_e32 v32, v20, v20
	v_fmac_f32_e32 v33, v22, v22
	v_add_f32_e32 v32, v32, v33
	v_mul_f32_e32 v33, v17, v17
	v_mul_f32_e32 v34, v19, v19
	v_fmac_f32_e32 v33, v16, v16
	v_fmac_f32_e32 v34, v18, v18
	v_add_f32_e32 v33, v33, v34
	v_add_f32_e32 v32, v32, v33
	v_mul_f32_e32 v33, v13, v13
	v_mul_f32_e32 v34, v15, v15
	v_fmac_f32_e32 v33, v12, v12
	v_fmac_f32_e32 v34, v14, v14
	v_add_f32_e32 v33, v33, v34
	v_add_f32_e32 v32, v32, v33
	v_mul_f32_e32 v33, v9, v9
	v_mul_f32_e32 v34, v11, v11
	v_fmac_f32_e32 v33, v8, v8
	v_fmac_f32_e32 v34, v10, v10
	v_add_f32_e32 v33, v33, v34
	v_add_f32_e32 v32, v32, v33
	s_nop 1
	v_mov_b32_dpp v33, v32 quad_perm:[1,0,3,2] row_mask:0xf bank_mask:0xf
	v_lshl_add_u64 v[50:51], v[50:51], 0, s[80:81]
	v_lshl_add_u64 v[52:53], v[52:53], 0, s[84:85]
	s_cmp_ge_i32 s2, s12
	s_waitcnt lgkmcnt(0)
	v_add_f32_e32 v32, v32, v33
	s_nop 1
	v_mov_b32_dpp v33, v32 quad_perm:[2,3,0,1] row_mask:0xf bank_mask:0xf
	s_waitcnt lgkmcnt(0)
	v_add_f32_e32 v32, v32, v33
	s_nop 1
	v_mov_b32_dpp v33, v32 row_half_mirror row_mask:0xf bank_mask:0xf
	s_waitcnt lgkmcnt(0)
	v_add_f32_e32 v32, v32, v33
	s_nop 1
	v_mov_b32_dpp v33, v32 row_mirror row_mask:0xf bank_mask:0xf
	s_waitcnt lgkmcnt(0)
	v_add_f32_e32 v32, v32, v33
	v_mov_b32_e32 v33, v32
	s_nop 1
	v_permlane16_swap_b32_e32 v32, v33
	s_waitcnt lgkmcnt(0)
	v_add_f32_e32 v32, v32, v33
	v_mov_b32_e32 v33, v32
	s_nop 1
	v_permlane32_swap_b32_e32 v32, v33
	v_add_f32_e32 v32, v32, v33
	v_fmamk_f32 v32, v32, 0x3a800000, v196
	v_cmp_gt_f32_e32 vcc, s35, v32
	v_mul_f32_e32 v33, 0x4b800000, v32
	s_nop 0
	v_cndmask_b32_e32 v32, v32, v33, vcc
	v_rsq_f32_e32 v32, v32
	s_nop 0
	v_mul_f32_e32 v33, 0x45800000, v32
	v_cndmask_b32_e32 v32, v32, v33, vcc
	v_pk_mul_f32 v[20:21], v[20:21], v[32:33] op_sel_hi:[1,0]
	v_pk_mul_f32 v[22:23], v[22:23], v[32:33] op_sel_hi:[1,0]
	v_pk_mul_f32 v[16:17], v[16:17], v[32:33] op_sel_hi:[1,0]
	v_pk_mul_f32 v[18:19], v[18:19], v[32:33] op_sel_hi:[1,0]
	v_pk_fma_f32 v[22:23], v[56:57], v[22:23], v[2:3]
	v_pk_fma_f32 v[20:21], v[54:55], v[20:21], v[0:1]
	v_pk_fma_f32 v[34:35], v[58:59], v[18:19], v[6:7]
	v_pk_fma_f32 v[36:37], v[62:63], v[16:17], v[4:5]
	v_cvt_pk_bf16_f32 v16, v20, v21
	v_cvt_pk_bf16_f32 v17, v22, v23
	v_cvt_pk_bf16_f32 v18, v36, v37
	v_cvt_pk_bf16_f32 v19, v34, v35
	global_store_dwordx4 v[42:43], v[16:19], off offset:2048
	v_pk_mul_f32 v[12:13], v[12:13], v[32:33] op_sel_hi:[1,0]
	v_pk_mul_f32 v[14:15], v[14:15], v[32:33] op_sel_hi:[1,0]
	v_mov_b32_e32 v16, v113
	v_mov_b32_e32 v17, v113
	v_cvt_pk_fp8_f32 v16, v20, v21
	v_cvt_pk_fp8_f32 v17, v36, v37
	v_pk_mul_f32 v[8:9], v[8:9], v[32:33] op_sel_hi:[1,0]
	v_pk_mul_f32 v[10:11], v[10:11], v[32:33] op_sel_hi:[1,0]
	v_cvt_pk_fp8_f32 v16, v22, v23 op_sel:[0,0,1]
	v_cvt_pk_fp8_f32 v17, v34, v35 op_sel:[0,0,1]
	s_waitcnt vmcnt(1)
	v_pk_fma_f32 v[14:15], v[64:65], v[14:15], v[30:31]
	v_pk_fma_f32 v[12:13], v[66:67], v[12:13], v[28:29]
	v_pk_fma_f32 v[18:19], v[70:71], v[8:9], v[24:25]
	global_store_dwordx2 v[40:41], v[16:17], off offset:1024
	v_pk_fma_f32 v[16:17], v[68:69], v[10:11], v[26:27]
	v_cvt_pk_bf16_f32 v8, v12, v13
	v_cvt_pk_bf16_f32 v9, v14, v15
	v_cvt_pk_bf16_f32 v10, v18, v19
	v_cvt_pk_bf16_f32 v11, v16, v17
	global_store_dwordx4 v[42:43], v[8:11], off offset:3072
	s_nop 1
	v_mov_b32_e32 v8, v113
	v_mov_b32_e32 v9, v113
	v_cvt_pk_fp8_f32 v8, v12, v13
	v_cvt_pk_fp8_f32 v9, v18, v19
	v_cvt_pk_fp8_f32 v8, v14, v15 op_sel:[0,0,1]
	v_cvt_pk_fp8_f32 v9, v16, v17 op_sel:[0,0,1]
	global_store_dwordx2 v[40:41], v[8:9], off offset:1536
	s_cbranch_scc1 .LBB0_153

.LBB0_151:
	s_waitcnt vmcnt(0)
	v_mul_f32_e32 v72, v45, v45
	v_mul_f32_e32 v73, v47, v47
	v_fmac_f32_e32 v72, v44, v44
	v_fmac_f32_e32 v73, v46, v46
	v_add_f32_e32 v72, v72, v73
	v_mul_f32_e32 v73, v41, v41
	v_mul_f32_e32 v74, v43, v43
	v_fmac_f32_e32 v73, v40, v40
	v_fmac_f32_e32 v74, v42, v42
	v_add_f32_e32 v73, v73, v74
	v_add_f32_e32 v72, v72, v73
	s_waitcnt vmcnt(4)
	v_mul_f32_e32 v73, v37, v37
	v_mul_f32_e32 v74, v39, v39
	v_fmac_f32_e32 v73, v36, v36
	v_fmac_f32_e32 v74, v38, v38
	v_add_f32_e32 v73, v73, v74
	v_add_f32_e32 v72, v72, v73
	v_mul_f32_e32 v73, v33, v33
	v_mul_f32_e32 v74, v35, v35
	v_fmac_f32_e32 v73, v32, v32
	v_fmac_f32_e32 v74, v34, v34
	v_add_f32_e32 v73, v73, v74
	v_add_f32_e32 v72, v72, v73
	s_nop 1
	v_mov_b32_dpp v73, v72 quad_perm:[1,0,3,2] row_mask:0xf bank_mask:0xf
	s_and_b64 s[14:15], s[38:39], exec
	s_mov_b32 s7, s4
	s_cselect_b32 s4, 16, s6
	s_mov_b32 s6, 0x17dd9000
	s_waitcnt lgkmcnt(0)
	v_add_f32_e32 v72, v72, v73
	s_nop 1
	v_mov_b32_dpp v73, v72 quad_perm:[2,3,0,1] row_mask:0xf bank_mask:0xf
	s_cmp_eq_u32 s4, s7
	s_waitcnt lgkmcnt(0)
	v_add_f32_e32 v72, v72, v73
	s_nop 1
	v_mov_b32_dpp v73, v72 row_half_mirror row_mask:0xf bank_mask:0xf
	s_waitcnt lgkmcnt(0)
	v_add_f32_e32 v72, v72, v73
	s_nop 1
	v_mov_b32_dpp v73, v72 row_mirror row_mask:0xf bank_mask:0xf
	s_waitcnt lgkmcnt(0)
	v_add_f32_e32 v72, v72, v73
	v_mov_b32_e32 v73, v72
	s_nop 1
	v_permlane16_swap_b32_e32 v72, v73
	s_waitcnt lgkmcnt(0)
	v_add_f32_e32 v72, v72, v73
	v_mov_b32_e32 v73, v72
	s_nop 1
	v_permlane32_swap_b32_e32 v72, v73
	v_add_f32_e32 v72, v72, v73
	v_fmamk_f32 v72, v72, 0x3a800000, v196
	v_cmp_gt_f32_e32 vcc, s35, v72
	v_mul_f32_e32 v73, 0x4b800000, v72
	s_nop 0
	v_cndmask_b32_e32 v72, v72, v73, vcc
	v_rsq_f32_e32 v72, v72
	s_nop 0
	v_mul_f32_e32 v73, 0x45800000, v72
	v_cndmask_b32_e32 v72, v72, v73, vcc
	v_pk_mul_f32 v[42:43], v[42:43], v[72:73] op_sel_hi:[1,0]
	v_pk_mul_f32 v[44:45], v[44:45], v[72:73] op_sel_hi:[1,0]
	v_pk_mul_f32 v[46:47], v[46:47], v[72:73] op_sel_hi:[1,0]
	v_pk_mul_f32 v[40:41], v[40:41], v[72:73] op_sel_hi:[1,0]
	v_pk_fma_f32 v[78:79], v[58:59], v[42:43], v[6:7]
	v_lshl_add_u64 v[42:43], s[94:95], 0, v[52:53]
	v_pk_fma_f32 v[74:75], v[56:57], v[46:47], v[2:3]
	v_pk_fma_f32 v[76:77], v[54:55], v[44:45], v[0:1]
	v_pk_fma_f32 v[40:41], v[62:63], v[40:41], v[4:5]
	v_add_co_u32_e32 v42, vcc, s6, v42
	v_cvt_pk_bf16_f32 v44, v76, v77
	v_cvt_pk_bf16_f32 v45, v74, v75
	v_cvt_pk_bf16_f32 v46, v40, v41
	v_cvt_pk_bf16_f32 v47, v78, v79
	v_addc_co_u32_e32 v43, vcc, 0, v43, vcc
	global_store_dwordx4 v[42:43], v[44:47], off
	s_mov_b32 s6, 0x711d9000
	v_pk_mul_f32 v[36:37], v[36:37], v[72:73] op_sel_hi:[1,0]
	v_mov_b32_e32 v44, v113
	v_mov_b32_e32 v45, v113
	v_cvt_pk_fp8_f32 v44, v76, v77
	v_cvt_pk_fp8_f32 v45, v40, v41
	v_lshl_add_u64 v[40:41], s[94:95], 0, v[50:51]
	v_add_co_u32_e32 v40, vcc, s6, v40
	v_cvt_pk_fp8_f32 v44, v74, v75 op_sel:[0,0,1]
	v_cvt_pk_fp8_f32 v45, v78, v79 op_sel:[0,0,1]
	v_addc_co_u32_e32 v41, vcc, 0, v41, vcc
	v_pk_mul_f32 v[38:39], v[38:39], v[72:73] op_sel_hi:[1,0]
	v_pk_mul_f32 v[32:33], v[32:33], v[72:73] op_sel_hi:[1,0]
	v_pk_mul_f32 v[34:35], v[34:35], v[72:73] op_sel_hi:[1,0]
	global_store_dwordx2 v[40:41], v[44:45], off
	s_waitcnt vmcnt(2)
	v_pk_fma_f32 v[38:39], v[64:65], v[38:39], v[30:31]
	v_pk_fma_f32 v[36:37], v[66:67], v[36:37], v[28:29]
	v_pk_fma_f32 v[44:45], v[68:69], v[34:35], v[26:27]
	v_pk_fma_f32 v[46:47], v[70:71], v[32:33], v[24:25]
	v_cvt_pk_bf16_f32 v32, v36, v37
	v_cvt_pk_bf16_f32 v33, v38, v39
	v_cvt_pk_bf16_f32 v34, v46, v47
	v_cvt_pk_bf16_f32 v35, v44, v45
	global_store_dwordx4 v[42:43], v[32:35], off offset:1024
	s_nop 1
	v_mov_b32_e32 v32, v113
	v_mov_b32_e32 v33, v113
	v_cvt_pk_fp8_f32 v32, v36, v37
	v_cvt_pk_fp8_f32 v33, v46, v47
	v_cvt_pk_fp8_f32 v32, v38, v39 op_sel:[0,0,1]
	v_cvt_pk_fp8_f32 v33, v44, v45 op_sel:[0,0,1]
	global_store_dwordx2 v[40:41], v[32:33], off offset:512
	s_cbranch_scc1 .LBB0_148
	s_mul_i32 s6, s4, 0x6000
	s_mul_hi_i32 s7, s4, 0x6000
	s_add_u32 s6, s60, s6
	s_addc_u32 s7, s63, s7
	v_lshl_add_u64 v[44:45], v[60:61], 2, s[6:7]
	v_add_co_u32_e32 v24, vcc, 0x1000, v44
	global_load_dwordx4 v[0:3], v[48:49], off offset:16
	global_load_dwordx4 v[4:7], v[48:49], off
	v_addc_co_u32_e32 v25, vcc, 0, v45, vcc
	v_lshl_add_u64 v[36:37], v[44:45], 0, s[84:85]
	global_load_dwordx4 v[24:27], v[24:25], off
	s_nop 0
	global_load_dwordx4 v[28:31], v[36:37], off offset:16
	s_waitcnt vmcnt(1)
	v_pk_add_f32 v[26:27], v[26:27], 1.0 op_sel_hi:[1,0]
	v_pk_add_f32 v[24:25], v[24:25], 1.0 op_sel_hi:[1,0]
	v_pk_mul_f32 v[56:57], v[6:7], v[26:27]
	v_pk_mul_f32 v[54:55], v[4:5], v[24:25]
	s_waitcnt vmcnt(0)
	v_pk_add_f32 v[4:5], v[30:31], 1.0 op_sel_hi:[1,0]
	v_pk_add_f32 v[6:7], v[28:29], 1.0 op_sel_hi:[1,0]
	v_pk_mul_f32 v[58:59], v[2:3], v[4:5]
	v_pk_mul_f32 v[62:63], v[0:1], v[6:7]
	global_load_dwordx4 v[4:7], v[44:45], off offset:16
	global_load_dwordx4 v[0:3], v[44:45], off
	global_load_dwordx4 v[24:27], v[48:49], off offset:2064
	global_load_dwordx4 v[28:31], v[48:49], off offset:2048
	global_load_dwordx4 v[32:35], v[36:37], off offset:2064
	s_nop 0
	global_load_dwordx4 v[36:39], v[36:37], off offset:2048
	s_waitcnt vmcnt(0)
	v_pk_add_f32 v[38:39], v[38:39], 1.0 op_sel_hi:[1,0]
	v_pk_add_f32 v[36:37], v[36:37], 1.0 op_sel_hi:[1,0]
	v_pk_mul_f32 v[64:65], v[30:31], v[38:39]
	v_pk_mul_f32 v[66:67], v[28:29], v[36:37]
	v_pk_add_f32 v[28:29], v[34:35], 1.0 op_sel_hi:[1,0]
	v_pk_add_f32 v[30:31], v[32:33], 1.0 op_sel_hi:[1,0]
	v_pk_mul_f32 v[68:69], v[26:27], v[28:29]
	v_pk_mul_f32 v[70:71], v[24:25], v[30:31]
	global_load_dwordx4 v[24:27], v[44:45], off offset:2064
	global_load_dwordx4 v[28:31], v[44:45], off offset:2048
	s_branch .LBB0_148

.LBB0_343:
	s_add_i32 s70, s6, -3
	s_mul_hi_i32 s2, s70, 0x78787879
	s_lshr_b32 s7, s2, 31
	s_ashr_i32 s2, s2, 11
	s_add_i32 s2, s2, s7
	s_mulk_i32 s2, 0x1100
	s_sub_i32 s7, s70, s2
	s_cmpk_lt_i32 s7, 0x100
	s_movk_i32 s2, 0x1100
	s_cselect_b32 s2, 0x100, s2
	s_cselect_b32 s12, 0, 0x100
	s_add_i32 s13, s7, -2
	s_add_i32 s15, s2, -1
	s_add_i32 s14, s7, -1
	s_min_i32 s13, s13, s15
	s_min_i32 s14, s14, s15
	s_cmp_gt_i32 s7, s12
	s_cselect_b64 s[38:39], -1, 0
	s_and_b64 s[26:27], s[38:39], exec
	s_cselect_b32 s13, s13, s12
	s_cselect_b32 s14, s14, s12
	s_sub_i32 s13, s13, s7
	s_add_i32 s26, s70, s13
	s_ashr_i32 s27, s26, 31
	s_lshl_b64 s[26:27], s[26:27], 9
	v_lshl_add_u64 v[82:83], v[66:67], 0, s[26:27]
	global_load_dwordx2 v[94:95], v[82:83], off
	v_lshl_add_u64 v[82:83], v[68:69], 0, s[26:27]
	s_sub_i32 s13, s14, s7
	global_load_dwordx2 v[104:105], v[82:83], off
	v_lshl_add_u64 v[82:83], v[70:71], 0, s[26:27]
	s_add_i32 s26, s70, s13
	s_ashr_i32 s27, s26, 31
	s_lshl_b64 s[26:27], s[26:27], 9
	s_min_i32 s13, s7, s15
	global_load_dwordx2 v[106:107], v[82:83], off
	v_lshl_add_u64 v[82:83], v[66:67], 0, s[26:27]
	s_cmp_lt_i32 s7, s12
	global_load_dwordx2 v[108:109], v[82:83], off
	v_lshl_add_u64 v[82:83], v[68:69], 0, s[26:27]
	s_cselect_b64 s[40:41], -1, 0
	global_load_dwordx2 v[110:111], v[82:83], off
	v_lshl_add_u64 v[82:83], v[70:71], 0, s[26:27]
	s_and_b64 s[26:27], s[40:41], exec
	s_cselect_b32 s13, s12, s13
	s_sub_i32 s13, s13, s7
	s_add_i32 s26, s70, s13
	s_ashr_i32 s27, s26, 31
	s_or_b32 s14, s7, 1
	s_lshl_b64 s[26:27], s[26:27], 9
	s_min_i32 s13, s14, s15
	s_cmp_lt_i32 s14, s12
	global_load_dwordx2 v[114:115], v[82:83], off
	v_lshl_add_u64 v[82:83], v[66:67], 0, s[26:27]
	s_cselect_b32 s13, s12, s13
	global_load_dwordx2 v[116:117], v[82:83], off
	v_lshl_add_u64 v[82:83], v[68:69], 0, s[26:27]
	s_sub_i32 s13, s13, s7
	global_load_dwordx2 v[118:119], v[82:83], off
	v_lshl_add_u64 v[82:83], v[70:71], 0, s[26:27]
	s_add_i32 s26, s70, s13
	s_ashr_i32 s27, s26, 31
	s_or_b32 s25, s7, 2
	s_lshl_b64 s[42:43], s[26:27], 9
	s_min_i32 s13, s25, s15
	global_load_dwordx2 v[120:121], v[82:83], off
	v_add_u32_e32 v82, s70, v138
	s_cmp_lt_i32 s25, s12
	v_ashrrev_i32_e32 v83, 31, v82
	s_cselect_b32 s13, s12, s13
	v_lshlrev_b64 v[86:87], 9, v[82:83]
	s_sub_i32 s13, s13, s7
	v_lshl_add_u64 v[84:85], v[66:67], 0, s[42:43]
	v_lshl_add_u64 v[86:87], v[74:75], 0, v[86:87]
	s_add_i32 s26, s70, s13
	global_load_ushort v112, v[86:87], off
	global_load_dwordx2 v[126:127], v[84:85], off
	v_lshl_add_u64 v[84:85], v[68:69], 0, s[42:43]
	s_ashr_i32 s27, s26, 31
	global_load_dwordx2 v[140:141], v[84:85], off
	v_lshl_add_u64 v[84:85], v[70:71], 0, s[42:43]
	s_lshl_b64 s[26:27], s[26:27], 9
	global_load_dwordx2 v[142:143], v[84:85], off
	v_lshl_add_u64 v[84:85], v[66:67], 0, s[26:27]
	global_load_dwordx2 v[144:145], v[84:85], off
	v_lshl_add_u64 v[84:85], v[68:69], 0, s[26:27]
	global_load_dwordx2 v[146:147], v[84:85], off
	v_lshl_add_u64 v[84:85], v[70:71], 0, s[26:27]
	s_or_b32 s26, s7, 3
	s_min_i32 s13, s26, s15
	s_cmp_lt_i32 s26, s12
	s_cselect_b32 s13, s12, s13
	s_sub_i32 s13, s13, s7
	s_add_i32 s28, s70, s13
	s_ashr_i32 s29, s28, 31
	s_add_i32 s27, s7, 4
	s_lshl_b64 s[28:29], s[28:29], 9
	s_min_i32 s13, s27, s15
	s_cmp_lt_i32 s27, s12
	global_load_dwordx2 v[148:149], v[84:85], off
	v_lshl_add_u64 v[84:85], v[66:67], 0, s[28:29]
	s_cselect_b32 s13, s12, s13
	global_load_dwordx2 v[170:171], v[84:85], off
	v_lshl_add_u64 v[84:85], v[68:69], 0, s[28:29]
	s_sub_i32 s13, s13, s7
	global_load_dwordx2 v[172:173], v[84:85], off
	v_lshl_add_u64 v[84:85], v[70:71], 0, s[28:29]
	s_add_i32 s28, s70, s13
	s_ashr_i32 s29, s28, 31
	s_add_i32 s13, s7, 5
	s_lshl_b64 s[28:29], s[28:29], 9
	s_min_i32 s15, s13, s15
	s_cmp_lt_i32 s13, s12
	global_load_dwordx2 v[150:151], v[84:85], off
	v_lshl_add_u64 v[84:85], v[66:67], 0, s[28:29]
	s_cselect_b32 s15, s12, s15
	global_load_dwordx2 v[174:175], v[84:85], off
	v_lshl_add_u64 v[84:85], v[68:69], 0, s[28:29]
	s_sub_i32 s7, s15, s7
	global_load_dwordx2 v[176:177], v[84:85], off
	v_lshl_add_u64 v[84:85], v[70:71], 0, s[28:29]
	s_add_i32 s28, s70, s7
	s_ashr_i32 s29, s28, 31
	s_lshl_b64 s[28:29], s[28:29], 9
	global_load_dwordx2 v[178:179], v[84:85], off
	v_lshl_add_u64 v[84:85], v[66:67], 0, s[28:29]
	global_load_dwordx2 v[102:103], v[84:85], off
	v_lshl_add_u64 v[84:85], v[68:69], 0, s[28:29]
	s_ashr_i32 s71, s70, 31
	global_load_dwordx2 v[100:101], v[84:85], off
	v_lshl_add_u64 v[84:85], v[70:71], 0, s[28:29]
	s_lshl_b64 s[28:29], s[70:71], 9
	v_lshl_add_u64 v[96:97], v[72:73], 0, s[28:29]
	global_load_dwordx2 v[124:125], v[96:97], off
	global_load_dwordx2 v[98:99], v[84:85], off
	s_add_i32 s72, s6, -2
	s_ashr_i32 s73, s72, 31
	s_lshl_b64 s[28:29], s[72:73], 9
	v_lshl_add_u64 v[88:89], v[72:73], 0, s[28:29]
	global_load_dwordx2 v[122:123], v[88:89], off
	s_add_i32 s64, s6, -1
	s_ashr_i32 s65, s64, 31
	s_lshl_b64 s[28:29], s[64:65], 9
	s_ashr_i32 s7, s6, 31
	v_lshl_add_u64 v[86:87], v[72:73], 0, s[28:29]
	s_lshl_b64 s[28:29], s[6:7], 9
	s_cmp_ge_i32 s14, s12
	v_lshl_add_u64 v[84:85], v[72:73], 0, s[28:29]
	s_cselect_b64 s[28:29], -1, 0
	s_cmp_lt_i32 s14, s2
	s_cselect_b64 s[14:15], -1, 0
	s_waitcnt vmcnt(0)
	v_cndmask_b32_e64 v134, 0, v107, s[38:39]
	v_cndmask_b32_e64 v136, 0, v106, s[38:39]
	v_cndmask_b32_e64 v128, 0, v105, s[38:39]
	v_cndmask_b32_e64 v130, 0, v104, s[38:39]
	v_cndmask_b32_e64 v167, 0, v95, s[38:39]
	v_cndmask_b32_e64 v168, 0, v94, s[38:39]
	v_cndmask_b32_e64 v137, 0, v115, s[38:39]
	v_cndmask_b32_e64 v135, 0, v114, s[38:39]
	v_cndmask_b32_e64 v131, 0, v111, s[38:39]
	v_cndmask_b32_e64 v129, 0, v110, s[38:39]
	v_cndmask_b32_e64 v165, 0, v109, s[38:39]
	v_cndmask_b32_e64 v166, 0, v108, s[38:39]
	s_and_b64 s[38:39], s[28:29], s[14:15]
	s_cmp_ge_i32 s25, s12
	s_cselect_b64 s[14:15], -1, 0
	s_cmp_lt_i32 s25, s2
	s_cselect_b64 s[28:29], -1, 0
	v_cndmask_b32_e64 v157, v119, 0, s[40:41]
	v_cndmask_b32_e64 v161, v117, 0, s[40:41]
	v_cndmask_b32_e64 v132, 0, v143, s[38:39]
	v_cndmask_b32_e64 v156, 0, v142, s[38:39]
	v_cndmask_b32_e64 v119, 0, v141, s[38:39]
	v_cndmask_b32_e64 v159, 0, v140, s[38:39]
	v_cndmask_b32_e64 v117, 0, v127, s[38:39]
	v_cndmask_b32_e64 v163, 0, v126, s[38:39]
	s_and_b64 s[38:39], s[14:15], s[28:29]
	s_cmp_ge_i32 s26, s12
	s_cselect_b64 s[14:15], -1, 0
	s_cmp_lt_i32 s26, s2
	s_cselect_b64 s[28:29], -1, 0
	v_cndmask_b32_e64 v160, v118, 0, s[40:41]
	v_cndmask_b32_e64 v164, v116, 0, s[40:41]
	v_cndmask_b32_e64 v126, 0, v149, s[38:39]
	v_cndmask_b32_e64 v155, 0, v148, s[38:39]
	v_cndmask_b32_e64 v118, 0, v147, s[38:39]
	v_cndmask_b32_e64 v158, 0, v146, s[38:39]
	v_cndmask_b32_e64 v116, 0, v145, s[38:39]
	v_cndmask_b32_e64 v162, 0, v144, s[38:39]
	s_and_b64 s[38:39], s[14:15], s[28:29]
	s_cmp_ge_i32 s27, s12
	s_cselect_b64 s[14:15], -1, 0
	s_cmp_lt_i32 s27, s2
	s_cselect_b64 s[26:27], -1, 0
	v_cndmask_b32_e64 v151, 0, v151, s[38:39]
	v_cndmask_b32_e64 v152, 0, v150, s[38:39]
	v_cndmask_b32_e64 v153, 0, v173, s[38:39]
	v_cndmask_b32_e64 v154, 0, v172, s[38:39]
	v_cndmask_b32_e64 v133, 0, v171, s[38:39]
	v_cndmask_b32_e64 v127, 0, v170, s[38:39]
	s_and_b64 s[38:39], s[14:15], s[26:27]
	v_cndmask_b32_e64 v121, v121, 0, s[40:41]
	v_cndmask_b32_e64 v120, v120, 0, s[40:41]
	v_cndmask_b32_e64 v141, 0, v177, s[38:39]
	v_cndmask_b32_e64 v142, 0, v176, s[38:39]
	v_cndmask_b32_e64 v145, 0, v175, s[38:39]
	v_cndmask_b32_e64 v146, 0, v174, s[38:39]
	v_cndmask_b32_e64 v139, 0, v179, s[38:39]
	v_cndmask_b32_e64 v140, 0, v178, s[38:39]
	global_load_dwordx2 v[92:93], v[86:87], off
	global_load_dwordx2 v[90:91], v[84:85], off
	s_cmp_ge_i32 s13, s12
	s_cselect_b64 s[14:15], -1, 0
	v_lshlrev_b32_e32 v104, 16, v125
	v_and_b32_e32 v105, 0xffff0000, v125
	v_fma_f32 v94, |v104|, s33, 1.0
	v_rcp_f32_e32 v106, v94
	v_fma_f32 v94, |v105|, s33, 1.0
	v_rcp_f32_e32 v107, v94
	v_pk_mul_f32 v[108:109], v[104:105], v[104:105]
	v_cmp_gt_f32_e64 s[38:39], 0, v104
	v_mul_f32_e32 v94, 0xbf38aa3b, v108
	v_exp_f32_e32 v108, v94
	v_mov_b64_e32 v[94:95], s[86:87]
	v_pk_fma_f32 v[110:111], v[106:107], s[82:83], v[94:95] op_sel_hi:[1,0,0]
	v_mul_f32_e32 v109, 0xbf38aa3b, v109
	v_pk_fma_f32 v[110:111], v[106:107], v[110:111], s[96:97] op_sel_hi:[1,1,0]
	v_exp_f32_e32 v109, v109
	v_pk_fma_f32 v[110:111], v[106:107], v[110:111], s[30:31] op_sel_hi:[1,1,0]
	v_cmp_gt_f32_e64 s[40:41], 0, v105
	v_pk_fma_f32 v[110:111], v[106:107], v[110:111], s[36:37] op_sel_hi:[1,1,0]
	s_cmp_lt_i32 s13, s2
	v_pk_mul_f32 v[106:107], v[106:107], v[110:111]
	s_cselect_b64 s[12:13], -1, 0
	v_pk_mul_f32 v[106:107], v[108:109], v[106:107]
	s_mov_b32 s28, 0x358637bd
	v_pk_mul_f32 v[108:109], v[106:107], v[104:105]
	v_pk_fma_f32 v[104:105], v[106:107], v[104:105], v[104:105] neg_lo:[1,0,0] neg_hi:[1,0,0]
	s_mov_b32 s2, 0x3b800000
	v_cndmask_b32_e64 v111, v105, v109, s[40:41]
	v_cndmask_b32_e64 v110, v104, v108, s[38:39]
	v_lshlrev_b32_e32 v104, 16, v124
	v_and_b32_e32 v105, 0xffff0000, v124
	v_fma_f32 v106, |v104|, s33, 1.0
	v_fma_f32 v107, |v105|, s33, 1.0
	v_rcp_f32_e32 v106, v106
	v_rcp_f32_e32 v107, v107
	v_pk_mul_f32 v[108:109], v[104:105], v[104:105]
	v_cmp_gt_f32_e64 s[38:39], 0, v104
	v_mul_f32_e32 v108, 0xbf38aa3b, v108
	v_pk_fma_f32 v[114:115], v[106:107], s[82:83], v[94:95] op_sel_hi:[1,0,0]
	v_mul_f32_e32 v109, 0xbf38aa3b, v109
	v_exp_f32_e32 v108, v108
	v_pk_fma_f32 v[114:115], v[106:107], v[114:115], s[96:97] op_sel_hi:[1,1,0]
	v_exp_f32_e32 v109, v109
	v_pk_fma_f32 v[114:115], v[106:107], v[114:115], s[30:31] op_sel_hi:[1,1,0]
	v_cmp_gt_f32_e64 s[40:41], 0, v105
	v_pk_fma_f32 v[114:115], v[106:107], v[114:115], s[36:37] op_sel_hi:[1,1,0]
	v_readlane_b32 s26, v253, 48
	v_pk_mul_f32 v[106:107], v[106:107], v[114:115]
	v_readlane_b32 s27, v253, 49
	v_pk_mul_f32 v[106:107], v[108:109], v[106:107]
	v_lshlrev_b32_e32 v112, 16, v112
	v_pk_mul_f32 v[108:109], v[106:107], v[104:105]
	v_pk_fma_f32 v[104:105], v[106:107], v[104:105], v[104:105] neg_lo:[1,0,0] neg_hi:[1,0,0]
	v_mov_b32_e32 v107, v111
	v_cndmask_b32_e64 v114, v104, v108, s[38:39]
	v_lshlrev_b32_e32 v108, 16, v122
	v_cndmask_b32_e64 v115, v105, v109, s[40:41]
	v_fma_f32 v109, |v108|, s33, 1.0
	v_mov_b32_e32 v106, v115
	v_rcp_f32_e32 v109, v109
	v_mov_b32_e32 v104, v114
	v_mov_b32_e32 v105, v110
	v_pk_mul_f32 v[106:107], v[106:107], v[106:107]
	v_cmp_gt_f32_e64 s[38:39], 0, v108
	v_pk_fma_f32 v[104:105], v[104:105], v[104:105], v[106:107]
	s_nop 0
	v_add_f32_e32 v124, v104, v105
	v_mul_f32_e32 v105, v108, v108
	v_fmamk_f32 v104, v109, 0x3f07dc22, v199
	v_mul_f32_e32 v105, 0xbf38aa3b, v105
	v_fmaak_f32 v104, v109, v104, 0x3f35f0e3
	v_exp_f32_e32 v105, v105
	v_fmaak_f32 v104, v109, v104, 0xbe11a98e
	v_fmaak_f32 v104, v109, v104, 0x3e027906
	v_mul_f32_e32 v104, v109, v104
	v_mul_f32_e32 v104, v105, v104
	v_and_b32_e32 v105, 0xffff0000, v122
	v_fma_f32 v106, |v105|, s33, 1.0
	v_rcp_f32_e32 v106, v106
	v_mul_f32_e32 v107, v105, v105
	v_mul_f32_e32 v143, v104, v108
	v_fma_f32 v144, -v104, v108, v108
	v_fmamk_f32 v104, v106, 0x3f07dc22, v199
	v_mul_f32_e32 v107, 0xbf38aa3b, v107
	v_fmaak_f32 v104, v106, v104, 0x3f35f0e3
	v_exp_f32_e32 v107, v107
	v_fmaak_f32 v104, v106, v104, 0xbe11a98e
	v_fmaak_f32 v104, v106, v104, 0x3e027906
	v_mul_f32_e32 v104, v106, v104
	v_mul_f32_e32 v104, v107, v104
	v_mul_f32_e32 v147, v104, v105
	v_cmp_gt_f32_e64 s[40:41], 0, v105
	v_fma_f32 v148, -v104, v105, v105
	v_lshlrev_b32_e32 v104, 16, v123
	v_and_b32_e32 v105, 0xffff0000, v123
	v_fma_f32 v106, |v104|, s33, 1.0
	v_fma_f32 v107, |v105|, s33, 1.0
	v_rcp_f32_e32 v106, v106
	v_rcp_f32_e32 v107, v107
	v_pk_mul_f32 v[108:109], v[104:105], v[104:105]
	v_cmp_gt_f32_e64 s[42:43], 0, v104
	v_mul_f32_e32 v108, 0xbf38aa3b, v108
	v_pk_fma_f32 v[122:123], v[106:107], s[82:83], v[94:95] op_sel_hi:[1,0,0]
	v_mul_f32_e32 v109, 0xbf38aa3b, v109
	v_exp_f32_e32 v108, v108
	v_pk_fma_f32 v[122:123], v[106:107], v[122:123], s[96:97] op_sel_hi:[1,1,0]
	v_exp_f32_e32 v109, v109
	v_pk_fma_f32 v[122:123], v[106:107], v[122:123], s[30:31] op_sel_hi:[1,1,0]
	v_cmp_gt_f32_e64 s[46:47], 0, v105
	v_pk_fma_f32 v[122:123], v[106:107], v[122:123], s[36:37] op_sel_hi:[1,1,0]
	s_nop 1
	v_mov_b32_dpp v125, v124 quad_perm:[1,0,3,2] row_mask:0xf bank_mask:0xf
	v_pk_mul_f32 v[106:107], v[106:107], v[122:123]
	s_nop 0
	v_pk_mul_f32 v[106:107], v[108:109], v[106:107]
	s_nop 0
	v_pk_mul_f32 v[108:109], v[106:107], v[104:105]
	v_pk_fma_f32 v[104:105], v[106:107], v[104:105], v[104:105] neg_lo:[1,0,0] neg_hi:[1,0,0]
	v_cndmask_b32_e64 v106, v144, v143, s[38:39]
	v_cndmask_b32_e64 v105, v105, v109, s[46:47]
	v_cndmask_b32_e64 v104, v104, v108, s[42:43]
	v_cndmask_b32_e64 v108, v148, v147, s[40:41]
	v_mov_b32_e32 v109, v105
	v_mov_b32_e32 v107, v104
	v_pk_mul_f32 v[122:123], v[108:109], v[108:109]
	s_and_b64 s[38:39], s[14:15], s[12:13]
	v_pk_fma_f32 v[122:123], v[106:107], v[106:107], v[122:123]
	v_cndmask_b32_e64 v150, 0, v102, s[38:39]
	v_add_f32_e32 v107, v122, v123
	s_nop 1
	v_mov_b32_dpp v109, v107 quad_perm:[1,0,3,2] row_mask:0xf bank_mask:0xf
	s_waitcnt lgkmcnt(0)
	v_add_f32_e32 v122, v124, v125
	s_nop 1
	v_mov_b32_dpp v123, v122 quad_perm:[2,3,0,1] row_mask:0xf bank_mask:0xf
	v_cndmask_b32_e64 v149, 0, v103, s[38:39]
	v_cndmask_b32_e64 v148, 0, v100, s[38:39]
	s_waitcnt lgkmcnt(0)
	v_add_f32_e32 v107, v107, v109
	s_nop 1
	v_mov_b32_dpp v109, v107 quad_perm:[2,3,0,1] row_mask:0xf bank_mask:0xf
	s_waitcnt lgkmcnt(0)
	v_add_f32_e32 v122, v122, v123
	s_nop 1
	v_mov_b32_dpp v123, v122 row_half_mirror row_mask:0xf bank_mask:0xf
	v_cndmask_b32_e64 v147, 0, v101, s[38:39]
	v_cndmask_b32_e64 v144, 0, v98, s[38:39]
	s_waitcnt lgkmcnt(0)
	v_add_f32_e32 v107, v107, v109
	s_nop 1
	v_mov_b32_dpp v109, v107 row_half_mirror row_mask:0xf bank_mask:0xf
	s_waitcnt lgkmcnt(0)
	v_add_f32_e32 v122, v122, v123
	s_nop 1
	v_mov_b32_dpp v123, v122 row_mirror row_mask:0xf bank_mask:0xf
	v_cndmask_b32_e64 v143, 0, v99, s[38:39]
	v_lshlrev_b32_e32 v124, 16, v165
	s_waitcnt lgkmcnt(0)
	v_add_f32_e32 v102, v107, v109
	s_nop 1
	v_mov_b32_dpp v103, v102 row_mirror row_mask:0xf bank_mask:0xf
	s_waitcnt lgkmcnt(0)
	v_add_f32_e32 v107, v122, v123
	v_mov_b32_e32 v109, v107
	s_nop 1
	v_permlane16_swap_b32_e32 v107, v109
	v_and_b32_e32 v125, 0xffff0000, v165
	s_lshl_b64 s[12:13], s[70:71], 8
	s_waitcnt lgkmcnt(0)
	v_add_f32_e32 v100, v102, v103
	v_mov_b32_e32 v102, v100
	s_nop 1
	v_permlane16_swap_b32_e32 v100, v102
	s_waitcnt lgkmcnt(0)
	v_add_f32_e32 v101, v107, v109
	v_mov_b32_e32 v103, v101
	s_nop 1
	v_permlane32_swap_b32_e32 v101, v103
	s_waitcnt lgkmcnt(0)
	v_add_f32_e32 v100, v100, v102
	v_mov_b32_e32 v102, v100
	s_nop 1
	v_permlane32_swap_b32_e32 v100, v102
	v_pk_add_f32 v[102:103], v[100:101], v[102:103]
	v_mov_b64_e32 v[100:101], s[28:29]
	v_pk_fma_f32 v[102:103], v[102:103], s[2:3], v[100:101] op_sel_hi:[1,0,0]
	v_readlane_b32 s14, v253, 36
	v_mul_f32_e32 v107, 0x4b800000, v103
	v_cmp_gt_f32_e64 s[40:41], s35, v103
	v_cmp_gt_f32_e64 s[38:39], s35, v102
	v_readlane_b32 s15, v253, 37
	v_cndmask_b32_e64 v103, v103, v107, s[40:41]
	v_rsq_f32_e32 v103, v103
	s_nop 0
	v_mul_f32_e32 v98, 0x45800000, v103
	v_cndmask_b32_e64 v98, v103, v98, s[40:41]
	v_mul_f32_e32 v103, 0x4b800000, v102
	v_cndmask_b32_e64 v102, v102, v103, s[38:39]
	v_rsq_f32_e32 v107, v102
	s_waitcnt vmcnt(1)
	v_lshlrev_b32_e32 v102, 16, v92
	v_fma_f32 v103, |v102|, s33, 1.0
	v_pk_mul_f32 v[114:115], v[98:99], v[114:115] op_sel_hi:[0,1]
	v_pk_mul_f32 v[98:99], v[98:99], v[110:111] op_sel_hi:[0,1]
	v_rcp_f32_e32 v103, v103
	v_pk_mul_f32 v[114:115], v[60:61], v[114:115]
	v_pk_mul_f32 v[98:99], v[62:63], v[98:99]
	v_cvt_pk_bf16_f32 v114, v114, v115
	v_cvt_pk_bf16_f32 v115, v98, v99
	global_store_dwordx2 v[96:97], v[114:115], off
	v_mul_f32_e32 v97, v102, v102
	v_fmamk_f32 v96, v103, 0x3f07dc22, v199
	v_mul_f32_e32 v97, 0xbf38aa3b, v97
	v_fmaak_f32 v96, v103, v96, 0x3f35f0e3
	v_exp_f32_e32 v97, v97
	v_fmaak_f32 v96, v103, v96, 0xbe11a98e
	v_fmaak_f32 v96, v103, v96, 0x3e027906
	v_mul_f32_e32 v96, v103, v96
	v_and_b32_e32 v92, 0xffff0000, v92
	v_mul_f32_e32 v96, v97, v96
	v_fma_f32 v97, |v92|, s33, 1.0
	v_rcp_f32_e32 v97, v97
	v_mul_f32_e32 v98, v92, v92
	v_mul_f32_e32 v110, v96, v102
	v_fma_f32 v111, -v96, v102, v102
	v_fmamk_f32 v96, v97, 0x3f07dc22, v199
	v_mul_f32_e32 v98, 0xbf38aa3b, v98
	v_fmaak_f32 v96, v97, v96, 0x3f35f0e3
	v_exp_f32_e32 v98, v98
	v_fmaak_f32 v96, v97, v96, 0xbe11a98e
	v_fmaak_f32 v96, v97, v96, 0x3e027906
	v_mul_f32_e32 v96, v97, v96
	v_mul_f32_e32 v96, v98, v96
	v_mul_f32_e32 v114, v96, v92
	v_cmp_gt_f32_e64 s[42:43], 0, v92
	v_fma_f32 v115, -v96, v92, v92
	v_lshlrev_b32_e32 v92, 16, v93
	v_and_b32_e32 v93, 0xffff0000, v93
	v_fma_f32 v96, |v92|, s33, 1.0
	v_fma_f32 v97, |v93|, s33, 1.0
	v_rcp_f32_e32 v96, v96
	v_rcp_f32_e32 v97, v97
	v_pk_mul_f32 v[98:99], v[92:93], v[92:93]
	v_cmp_gt_f32_e64 s[40:41], 0, v102
	v_mul_f32_e32 v98, 0xbf38aa3b, v98
	v_pk_fma_f32 v[102:103], v[96:97], s[82:83], v[94:95] op_sel_hi:[1,0,0]
	v_mul_f32_e32 v99, 0xbf38aa3b, v99
	v_exp_f32_e32 v98, v98
	v_pk_fma_f32 v[102:103], v[96:97], v[102:103], s[96:97] op_sel_hi:[1,1,0]
	v_exp_f32_e32 v99, v99
	v_pk_fma_f32 v[102:103], v[96:97], v[102:103], s[30:31] op_sel_hi:[1,1,0]
	v_cmp_gt_f32_e64 s[46:47], 0, v92
	v_pk_fma_f32 v[102:103], v[96:97], v[102:103], s[36:37] op_sel_hi:[1,1,0]
	v_cmp_gt_f32_e64 s[48:49], 0, v93
	v_pk_mul_f32 v[96:97], v[96:97], v[102:103]
	v_mul_f32_e32 v109, 0x45800000, v107
	v_pk_mul_f32 v[96:97], v[98:99], v[96:97]
	s_nop 0
	v_pk_mul_f32 v[98:99], v[96:97], v[92:93]
	v_pk_fma_f32 v[92:93], v[96:97], v[92:93], v[92:93] neg_lo:[1,0,0] neg_hi:[1,0,0]
	v_cndmask_b32_e64 v96, v111, v110, s[40:41]
	v_cndmask_b32_e64 v93, v93, v99, s[48:49]
	v_cndmask_b32_e64 v92, v92, v98, s[46:47]
	v_cndmask_b32_e64 v98, v115, v114, s[42:43]
	v_mov_b32_e32 v99, v93
	v_pk_mul_f32 v[102:103], v[98:99], v[98:99]
	s_waitcnt vmcnt(1)
	v_lshlrev_b32_e32 v99, 16, v90
	v_fma_f32 v110, |v99|, s33, 1.0
	v_rcp_f32_e32 v110, v110
	v_mov_b32_e32 v97, v92
	v_pk_fma_f32 v[102:103], v[96:97], v[96:97], v[102:103]
	v_and_b32_e32 v90, 0xffff0000, v90
	v_add_f32_e32 v97, v102, v103
	v_mul_f32_e32 v103, v99, v99
	v_fmamk_f32 v102, v110, 0x3f07dc22, v199
	v_mul_f32_e32 v103, 0xbf38aa3b, v103
	v_fmaak_f32 v102, v110, v102, 0x3f35f0e3
	v_exp_f32_e32 v103, v103
	v_fmaak_f32 v102, v110, v102, 0xbe11a98e
	v_fmaak_f32 v102, v110, v102, 0x3e027906
	v_mul_f32_e32 v102, v110, v102
	v_mul_f32_e32 v102, v103, v102
	v_fma_f32 v103, |v90|, s33, 1.0
	v_rcp_f32_e32 v103, v103
	v_mul_f32_e32 v110, v90, v90
	v_mul_f32_e32 v115, v102, v99
	v_cmp_gt_f32_e64 s[40:41], 0, v99
	v_fma_f32 v99, -v102, v99, v99
	v_fmamk_f32 v102, v103, 0x3f07dc22, v199
	v_mul_f32_e32 v110, 0xbf38aa3b, v110
	v_fmaak_f32 v102, v103, v102, 0x3f35f0e3
	v_exp_f32_e32 v110, v110
	v_fmaak_f32 v102, v103, v102, 0xbe11a98e
	v_fmaak_f32 v102, v103, v102, 0x3e027906
	v_mul_f32_e32 v102, v103, v102
	v_mul_f32_e32 v102, v110, v102
	v_mul_f32_e32 v122, v102, v90
	v_cmp_gt_f32_e64 s[42:43], 0, v90
	v_fma_f32 v123, -v102, v90, v90
	v_lshlrev_b32_e32 v90, 16, v91
	v_and_b32_e32 v91, 0xffff0000, v91
	v_fma_f32 v102, |v90|, s33, 1.0
	v_fma_f32 v103, |v91|, s33, 1.0
	v_rcp_f32_e32 v102, v102
	v_rcp_f32_e32 v103, v103
	v_pk_mul_f32 v[110:111], v[90:91], v[90:91]
	v_cmp_gt_f32_e64 s[46:47], 0, v90
	v_mul_f32_e32 v110, 0xbf38aa3b, v110
	v_pk_fma_f32 v[94:95], v[102:103], s[82:83], v[94:95] op_sel_hi:[1,0,0]
	v_mul_f32_e32 v111, 0xbf38aa3b, v111
	v_exp_f32_e32 v110, v110
	v_pk_fma_f32 v[94:95], v[102:103], v[94:95], s[96:97] op_sel_hi:[1,1,0]
	v_exp_f32_e32 v111, v111
	v_pk_fma_f32 v[94:95], v[102:103], v[94:95], s[30:31] op_sel_hi:[1,1,0]
	v_cmp_gt_f32_e64 s[48:49], 0, v91
	v_pk_fma_f32 v[94:95], v[102:103], v[94:95], s[36:37] op_sel_hi:[1,1,0]
	s_nop 1
	v_mov_b32_dpp v114, v97 quad_perm:[1,0,3,2] row_mask:0xf bank_mask:0xf
	v_pk_mul_f32 v[94:95], v[102:103], v[94:95]
	s_waitcnt lgkmcnt(0)
	v_add_f32_e32 v97, v97, v114
	v_pk_mul_f32 v[94:95], v[110:111], v[94:95]
	v_lshlrev_b32_e32 v114, 16, v160
	v_pk_mul_f32 v[102:103], v[94:95], v[90:91]
	v_pk_fma_f32 v[90:91], v[94:95], v[90:91], v[90:91] neg_lo:[1,0,0] neg_hi:[1,0,0]
	v_cndmask_b32_e64 v94, v99, v115, s[40:41]
	v_cndmask_b32_e64 v91, v91, v103, s[48:49]
	v_cndmask_b32_e64 v90, v90, v102, s[46:47]
	v_cndmask_b32_e64 v102, v123, v122, s[42:43]
	v_mov_b32_e32 v103, v91
	v_mov_b32_e32 v95, v90
	v_pk_mul_f32 v[110:111], v[102:103], v[102:103]
	s_nop 1
	v_mov_b32_dpp v103, v97 quad_perm:[2,3,0,1] row_mask:0xf bank_mask:0xf
	v_pk_fma_f32 v[110:111], v[94:95], v[94:95], v[110:111]
	v_lshlrev_b32_e32 v122, 16, v166
	v_add_f32_e32 v95, v110, v111
	s_nop 1
	v_mov_b32_dpp v99, v95 quad_perm:[1,0,3,2] row_mask:0xf bank_mask:0xf
	s_waitcnt lgkmcnt(0)
	v_add_f32_e32 v97, v97, v103
	s_nop 1
	v_mov_b32_dpp v103, v97 row_half_mirror row_mask:0xf bank_mask:0xf
	v_cndmask_b32_e64 v110, v107, v109, s[38:39]
	v_mov_b32_e32 v111, v108
	s_waitcnt lgkmcnt(0)
	v_add_f32_e32 v95, v95, v99
	s_nop 1
	v_mov_b32_dpp v99, v95 quad_perm:[2,3,0,1] row_mask:0xf bank_mask:0xf
	s_waitcnt lgkmcnt(0)
	v_add_f32_e32 v97, v97, v103
	s_nop 1
	v_mov_b32_dpp v103, v97 row_mirror row_mask:0xf bank_mask:0xf
	v_mov_b32_e32 v107, v110
	v_pk_mul_f32 v[106:107], v[110:111], v[106:107]
	s_waitcnt lgkmcnt(0)
	v_add_f32_e32 v95, v95, v99
	s_nop 1
	v_mov_b32_dpp v99, v95 row_half_mirror row_mask:0xf bank_mask:0xf
	s_waitcnt lgkmcnt(0)
	v_add_f32_e32 v97, v97, v103
	v_mov_b32_e32 v103, v97
	s_nop 1
	v_permlane16_swap_b32_e32 v97, v103
	v_pk_mul_f32 v[104:105], v[104:105], v[110:111] op_sel_hi:[1,0]
	v_pk_mul_f32 v[106:107], v[60:61], v[106:107]
	s_waitcnt lgkmcnt(0)
	v_add_f32_e32 v95, v95, v99
	s_nop 1
	v_mov_b32_dpp v99, v95 row_mirror row_mask:0xf bank_mask:0xf
	s_waitcnt lgkmcnt(0)
	v_add_f32_e32 v109, v97, v103
	v_mov_b32_e32 v111, v109
	s_nop 1
	v_permlane32_swap_b32_e32 v109, v111
	s_waitcnt lgkmcnt(0)
	v_add_f32_e32 v95, v95, v99
	v_mov_b32_e32 v99, v95
	s_nop 1
	v_permlane16_swap_b32_e32 v95, v99
	v_pk_mul_f32 v[104:105], v[62:63], v[104:105]
	v_cvt_pk_bf16_f32 v106, v106, v107
	v_cvt_pk_bf16_f32 v107, v104, v105
	global_store_dwordx2 v[88:89], v[106:107], off
	s_waitcnt lgkmcnt(0)
	v_add_f32_e32 v108, v95, v99
	v_mov_b32_e32 v110, v108
	s_nop 1
	v_permlane32_swap_b32_e32 v108, v110
	v_pk_add_f32 v[108:109], v[108:109], v[110:111]
	v_mov_b32_e32 v89, v98
	v_pk_fma_f32 v[100:101], v[108:109], s[2:3], v[100:101] op_sel_hi:[1,0,0]
	v_and_b32_e32 v123, 0xffff0000, v166
	v_mul_f32_e32 v95, 0x4b800000, v101
	v_cmp_gt_f32_e64 s[38:39], s35, v101
	v_cmp_gt_f32_e64 s[40:41], s35, v100
	v_lshlrev_b32_e32 v108, 16, v164
	v_cndmask_b32_e64 v95, v101, v95, s[38:39]
	v_rsq_f32_e32 v95, v95
	v_and_b32_e32 v109, 0xffff0000, v164
	v_lshlrev_b32_e32 v110, 16, v161
	v_and_b32_e32 v111, 0xffff0000, v161
	v_mul_f32_e32 v88, 0x45800000, v95
	v_cndmask_b32_e64 v88, v95, v88, s[38:39]
	v_mov_b32_e32 v97, v88
	v_pk_mul_f32 v[96:97], v[88:89], v[96:97]
	v_pk_mul_f32 v[88:89], v[92:93], v[88:89] op_sel_hi:[1,0]
	v_mul_f32_e32 v92, 0x4b800000, v100
	v_cndmask_b32_e64 v92, v100, v92, s[40:41]
	v_rsq_f32_e32 v92, v92
	v_pk_mul_f32 v[96:97], v[60:61], v[96:97]
	v_pk_mul_f32 v[88:89], v[62:63], v[88:89]
	v_cvt_pk_bf16_f32 v96, v96, v97
	v_cvt_pk_bf16_f32 v97, v88, v89
	global_store_dwordx2 v[86:87], v[96:97], off
	v_mul_f32_e32 v86, 0x45800000, v92
	v_cndmask_b32_e64 v86, v92, v86, s[40:41]
	v_mov_b32_e32 v87, v102
	v_mov_b32_e32 v95, v86
	v_pk_mul_f32 v[88:89], v[86:87], v[94:95]
	v_pk_mul_f32 v[86:87], v[90:91], v[86:87] op_sel_hi:[1,0]
	v_pk_mul_f32 v[88:89], v[60:61], v[88:89]
	v_pk_mul_f32 v[86:87], v[62:63], v[86:87]
	v_cvt_pk_bf16_f32 v88, v88, v89
	v_cvt_pk_bf16_f32 v89, v86, v87
	global_store_dwordx2 v[84:85], v[88:89], off
	v_lshlrev_b32_e32 v84, 16, v168
	v_and_b32_e32 v85, 0xffff0000, v168
	v_lshlrev_b32_e32 v86, 16, v167
	v_and_b32_e32 v87, 0xffff0000, v167
	v_pk_fma_f32 v[86:87], v[2:3], v[86:87], 0 op_sel_hi:[1,1,0]
	v_pk_fma_f32 v[84:85], v[0:1], v[84:85], 0 op_sel_hi:[1,1,0]
	v_pk_fma_f32 v[86:87], v[14:15], v[124:125], v[86:87]
	v_pk_fma_f32 v[84:85], v[12:13], v[122:123], v[84:85]
	v_pk_fma_f32 v[88:89], v[22:23], v[110:111], v[86:87]
	v_pk_fma_f32 v[90:91], v[20:21], v[108:109], v[84:85]
	v_lshlrev_b32_e32 v84, 16, v163
	v_and_b32_e32 v85, 0xffff0000, v163
	v_lshlrev_b32_e32 v86, 16, v117
	v_and_b32_e32 v87, 0xffff0000, v117
	v_pk_fma_f32 v[92:93], v[32:33], v[84:85], v[90:91]
	v_pk_fma_f32 v[94:95], v[34:35], v[86:87], v[88:89]
	v_lshlrev_b32_e32 v88, 16, v162
	v_and_b32_e32 v89, 0xffff0000, v162
	v_pk_fma_f32 v[162:163], v[48:49], v[88:89], v[92:93]
	v_lshlrev_b32_e32 v90, 16, v116
	v_mul_f32_e32 v92, 0xbfb8aa3b, v162
	v_exp_f32_e32 v92, v92
	v_mul_f32_e32 v93, 0xbfb8aa3b, v163
	v_exp_f32_e32 v93, v93
	v_and_b32_e32 v91, 0xffff0000, v116
	v_pk_fma_f32 v[164:165], v[50:51], v[90:91], v[94:95]
	v_add_f32_e32 v92, 1.0, v92
	v_rcp_f32_e32 v166, v92
	v_add_f32_e32 v92, 1.0, v93
	v_mul_f32_e32 v93, 0xbfb8aa3b, v164
	v_exp_f32_e32 v93, v93
	v_mul_f32_e32 v94, 0xbfb8aa3b, v165
	v_exp_f32_e32 v94, v94
	v_rcp_f32_e32 v167, v92
	v_add_f32_e32 v92, 1.0, v93
	v_rcp_f32_e32 v168, v92
	v_add_f32_e32 v92, 1.0, v94
	v_rcp_f32_e32 v169, v92
	v_lshlrev_b32_e32 v92, 16, v130
	v_and_b32_e32 v93, 0xffff0000, v130
	v_lshlrev_b32_e32 v94, 16, v128
	v_and_b32_e32 v95, 0xffff0000, v128
	v_pk_fma_f32 v[94:95], v[6:7], v[94:95], 0 op_sel_hi:[1,1,0]
	v_pk_fma_f32 v[92:93], v[4:5], v[92:93], 0 op_sel_hi:[1,1,0]
	v_lshlrev_b32_e32 v128, 16, v129
	v_and_b32_e32 v129, 0xffff0000, v129
	v_lshlrev_b32_e32 v130, 16, v131
	v_and_b32_e32 v131, 0xffff0000, v131
	v_pk_fma_f32 v[92:93], v[24:25], v[128:129], v[92:93]
	v_pk_fma_f32 v[94:95], v[26:27], v[130:131], v[94:95]
	v_and_b32_e32 v115, 0xffff0000, v160
	v_lshlrev_b32_e32 v116, 16, v157
	v_and_b32_e32 v117, 0xffff0000, v157
	v_pk_fma_f32 v[96:97], v[46:47], v[116:117], v[94:95]
	v_pk_fma_f32 v[98:99], v[44:45], v[114:115], v[92:93]
	v_lshlrev_b32_e32 v92, 16, v159
	v_and_b32_e32 v93, 0xffff0000, v159
	v_lshlrev_b32_e32 v94, 16, v119
	v_and_b32_e32 v95, 0xffff0000, v119
	v_pk_fma_f32 v[100:101], v[36:37], v[92:93], v[98:99]
	v_pk_fma_f32 v[102:103], v[38:39], v[94:95], v[96:97]
	v_lshlrev_b32_e32 v96, 16, v158
	v_and_b32_e32 v97, 0xffff0000, v158
	v_pk_fma_f32 v[158:159], v[52:53], v[96:97], v[100:101]
	v_lshlrev_b32_e32 v98, 16, v118
	v_mul_f32_e32 v100, 0xbfb8aa3b, v158
	v_exp_f32_e32 v100, v100
	v_mul_f32_e32 v101, 0xbfb8aa3b, v159
	v_exp_f32_e32 v101, v101
	v_and_b32_e32 v99, 0xffff0000, v118
	v_pk_fma_f32 v[160:161], v[54:55], v[98:99], v[102:103]
	v_add_f32_e32 v100, 1.0, v100
	v_rcp_f32_e32 v170, v100
	v_add_f32_e32 v100, 1.0, v101
	v_mul_f32_e32 v101, 0xbfb8aa3b, v160
	v_exp_f32_e32 v101, v101
	v_mul_f32_e32 v102, 0xbfb8aa3b, v161
	v_exp_f32_e32 v102, v102
	v_rcp_f32_e32 v171, v100
	v_add_f32_e32 v100, 1.0, v101
	v_rcp_f32_e32 v172, v100
	v_add_f32_e32 v100, 1.0, v102
	v_rcp_f32_e32 v173, v100
	v_pk_mul_f32 v[164:165], v[164:165], v[168:169]
	v_pk_mul_f32 v[162:163], v[162:163], v[166:167]
	v_mov_b32_e32 v169, v165
	v_mov_b32_e32 v168, v163
	v_pk_mul_f32 v[160:161], v[160:161], v[172:173]
	v_pk_mul_f32 v[158:159], v[158:159], v[170:171]
	v_mov_b32_e32 v166, v162
	v_mov_b32_e32 v167, v164
	v_pk_mul_f32 v[168:169], v[168:169], v[168:169]
	v_mov_b32_e32 v170, v159
	v_mov_b32_e32 v171, v161
	v_pk_fma_f32 v[166:167], v[166:167], v[166:167], v[168:169]
	v_mov_b32_e32 v168, v158
	v_mov_b32_e32 v169, v160
	v_pk_mul_f32 v[170:171], v[170:171], v[170:171]
	v_lshlrev_b32_e32 v100, 16, v136
	v_pk_fma_f32 v[168:169], v[168:169], v[168:169], v[170:171]
	v_mov_b32_e32 v171, v166
	v_mov_b32_e32 v170, v168
	v_mov_b32_e32 v166, v169
	v_pk_add_f32 v[166:167], v[170:171], v[166:167]
	s_nop 1
	v_mov_b32_dpp v169, v167 quad_perm:[1,0,3,2] row_mask:0xf bank_mask:0xf
	s_nop 1
	v_mov_b32_dpp v168, v166 quad_perm:[1,0,3,2] row_mask:0xf bank_mask:0xf
	v_and_b32_e32 v101, 0xffff0000, v136
	v_lshlrev_b32_e32 v102, 16, v134
	v_and_b32_e32 v103, 0xffff0000, v134
	v_pk_fma_f32 v[102:103], v[10:11], v[102:103], 0 op_sel_hi:[1,1,0]
	s_waitcnt lgkmcnt(0)
	v_pk_add_f32 v[166:167], v[166:167], v[168:169]
	v_pk_fma_f32 v[100:101], v[8:9], v[100:101], 0 op_sel_hi:[1,1,0]
	v_lshlrev_b32_e32 v134, 16, v135
	v_and_b32_e32 v135, 0xffff0000, v135
	v_lshlrev_b32_e32 v136, 16, v137
	v_and_b32_e32 v137, 0xffff0000, v137
	s_nop 1
	v_mov_b32_dpp v169, v167 quad_perm:[2,3,0,1] row_mask:0xf bank_mask:0xf
	s_nop 1
	v_mov_b32_dpp v168, v166 quad_perm:[2,3,0,1] row_mask:0xf bank_mask:0xf
	v_pk_fma_f32 v[100:101], v[16:17], v[134:135], v[100:101]
	v_pk_fma_f32 v[102:103], v[18:19], v[136:137], v[102:103]
	v_lshlrev_b32_e32 v118, 16, v120
	v_and_b32_e32 v119, 0xffff0000, v120
	v_lshlrev_b32_e32 v120, 16, v121
	v_and_b32_e32 v121, 0xffff0000, v121
	v_pk_fma_f32 v[104:105], v[30:31], v[120:121], v[102:103]
	v_pk_fma_f32 v[106:107], v[28:29], v[118:119], v[100:101]
	v_lshlrev_b32_e32 v100, 16, v156
	v_and_b32_e32 v101, 0xffff0000, v156
	v_lshlrev_b32_e32 v102, 16, v132
	v_and_b32_e32 v103, 0xffff0000, v132
	v_pk_fma_f32 v[156:157], v[40:41], v[100:101], v[106:107]
	v_pk_fma_f32 v[174:175], v[42:43], v[102:103], v[104:105]
	v_lshlrev_b32_e32 v104, 16, v155
	v_and_b32_e32 v105, 0xffff0000, v155
	v_pk_fma_f32 v[156:157], v[56:57], v[104:105], v[156:157]
	v_lshlrev_b32_e32 v106, 16, v126
	v_and_b32_e32 v107, 0xffff0000, v126
	v_mul_f32_e32 v126, 0xbfb8aa3b, v156
	s_waitcnt lgkmcnt(0)
	v_pk_add_f32 v[166:167], v[166:167], v[168:169]
	v_exp_f32_e32 v126, v126
	v_mul_f32_e32 v132, 0xbfb8aa3b, v157
	s_nop 1
	v_mov_b32_dpp v169, v167 row_half_mirror row_mask:0xf bank_mask:0xf
	s_nop 1
	v_mov_b32_dpp v168, v166 row_half_mirror row_mask:0xf bank_mask:0xf
	v_exp_f32_e32 v132, v132
	v_add_f32_e32 v126, 1.0, v126
	v_pk_fma_f32 v[174:175], v[58:59], v[106:107], v[174:175]
	v_rcp_f32_e32 v170, v126
	v_add_f32_e32 v126, 1.0, v132
	s_waitcnt lgkmcnt(0)
	v_pk_add_f32 v[166:167], v[166:167], v[168:169]
	v_rcp_f32_e32 v171, v126
	v_mul_f32_e32 v126, 0xbfb8aa3b, v174
	s_nop 1
	v_mov_b32_dpp v169, v167 row_mirror row_mask:0xf bank_mask:0xf
	s_nop 1
	v_mov_b32_dpp v168, v166 row_mirror row_mask:0xf bank_mask:0xf
	v_exp_f32_e32 v126, v126
	v_mul_f32_e32 v132, 0xbfb8aa3b, v175
	v_exp_f32_e32 v132, v132
	v_pk_mul_f32 v[156:157], v[156:157], v[170:171]
	v_add_f32_e32 v126, 1.0, v126
	s_waitcnt lgkmcnt(0)
	v_pk_add_f32 v[166:167], v[166:167], v[168:169]
	v_rcp_f32_e32 v172, v126
	v_add_f32_e32 v126, 1.0, v132
	v_pk_add_f32 v[166:167], v[166:167], s[28:29] op_sel_hi:[1,0]
	v_rcp_f32_e32 v173, v126
	v_mul_f32_e32 v126, 0x4b800000, v167
	v_cmp_gt_f32_e64 s[38:39], s35, v167
	v_cmp_gt_f32_e64 s[40:41], s35, v166
	v_pk_mul_f32 v[170:171], v[174:175], v[172:173]
	v_cndmask_b32_e64 v126, v167, v126, s[38:39]
	v_rsq_f32_e32 v126, v126
	v_lshl_add_u64 v[172:173], s[12:13], 0, v[64:65]
	v_pk_fma_f32 v[122:123], v[0:1], v[122:123], 0 op_sel_hi:[1,1,0]
	v_lshlrev_b64 v[168:169], 1, v[172:173]
	v_mul_f32_e32 v132, 0x45800000, v126
	v_cndmask_b32_e64 v126, v126, v132, s[38:39]
	v_mul_f32_e32 v132, 0x4b800000, v166
	v_cndmask_b32_e64 v132, v166, v132, s[40:41]
	v_rsq_f32_e32 v132, v132
	v_mul_f32_e32 v126, 0x3e000000, v126
	v_pk_mul_f32 v[162:163], v[162:163], v[126:127] op_sel_hi:[1,0]
	v_pk_mul_f32 v[164:165], v[164:165], v[126:127] op_sel_hi:[1,0]
	v_mul_f32_e32 v126, 0x45800000, v132
	v_cndmask_b32_e64 v126, v132, v126, s[40:41]
	v_pk_mul_f32 v[158:159], v[158:159], v[126:127] op_sel_hi:[1,0]
	v_pk_mul_f32 v[160:161], v[160:161], v[126:127] op_sel_hi:[1,0]
	v_pk_fma_f32 v[122:123], v[12:13], v[108:109], v[122:123]
	v_cvt_pk_bf16_f32 v158, v158, v159
	v_cvt_pk_bf16_f32 v159, v160, v161
	v_lshl_add_u64 v[160:161], s[14:15], 0, v[168:169]
	v_pk_fma_f32 v[122:123], v[20:21], v[84:85], v[122:123]
	global_store_dwordx2 v[160:161], v[158:159], off
	v_cvt_pk_bf16_f32 v156, v156, v157
	v_cvt_pk_bf16_f32 v157, v170, v171
	v_lshl_add_u64 v[158:159], s[26:27], 0, v[168:169]
	v_pk_fma_f32 v[122:123], v[32:33], v[88:89], v[122:123]
	v_lshlrev_b32_e32 v126, 16, v127
	v_and_b32_e32 v127, 0xffff0000, v127
	global_store_dwordx2 v[158:159], v[156:157], off
	v_pk_fma_f32 v[156:157], v[48:49], v[126:127], v[122:123]
	v_pk_fma_f32 v[124:125], v[2:3], v[124:125], 0 op_sel_hi:[1,1,0]
	v_mul_f32_e32 v122, 0xbfb8aa3b, v156
	v_exp_f32_e32 v122, v122
	v_mul_f32_e32 v123, 0xbfb8aa3b, v157
	v_pk_fma_f32 v[124:125], v[14:15], v[110:111], v[124:125]
	v_exp_f32_e32 v123, v123
	v_pk_fma_f32 v[124:125], v[22:23], v[86:87], v[124:125]
	v_lshlrev_b32_e32 v132, 16, v133
	v_pk_fma_f32 v[124:125], v[34:35], v[90:91], v[124:125]
	v_and_b32_e32 v133, 0xffff0000, v133
	v_pk_fma_f32 v[158:159], v[50:51], v[132:133], v[124:125]
	v_add_f32_e32 v122, 1.0, v122
	v_rcp_f32_e32 v160, v122
	v_add_f32_e32 v122, 1.0, v123
	v_mul_f32_e32 v123, 0xbfb8aa3b, v158
	v_exp_f32_e32 v123, v123
	v_mul_f32_e32 v124, 0xbfb8aa3b, v159
	v_exp_f32_e32 v124, v124
	v_lshl_add_u64 v[172:173], s[18:19], 0, v[168:169]
	v_cvt_pk_bf16_f32 v162, v162, v163
	v_cvt_pk_bf16_f32 v163, v164, v165
	v_rcp_f32_e32 v161, v122
	v_add_f32_e32 v122, 1.0, v123
	global_store_dwordx2 v[172:173], v[162:163], off
	v_rcp_f32_e32 v162, v122
	v_add_f32_e32 v122, 1.0, v124
	v_pk_fma_f32 v[124:125], v[4:5], v[128:129], 0 op_sel_hi:[1,1,0]
	v_rcp_f32_e32 v163, v122
	v_pk_fma_f32 v[124:125], v[24:25], v[114:115], v[124:125]
	v_pk_fma_f32 v[122:123], v[6:7], v[130:131], 0 op_sel_hi:[1,1,0]
	v_pk_fma_f32 v[124:125], v[44:45], v[92:93], v[124:125]
	v_pk_fma_f32 v[122:123], v[26:27], v[116:117], v[122:123]
	v_pk_fma_f32 v[128:129], v[36:37], v[96:97], v[124:125]
	v_lshlrev_b32_e32 v124, 16, v154
	v_and_b32_e32 v125, 0xffff0000, v154
	v_pk_fma_f32 v[154:155], v[52:53], v[124:125], v[128:129]
	v_pk_fma_f32 v[122:123], v[46:47], v[94:95], v[122:123]
	v_mul_f32_e32 v128, 0xbfb8aa3b, v154
	v_exp_f32_e32 v128, v128
	v_pk_fma_f32 v[122:123], v[38:39], v[98:99], v[122:123]
	v_lshlrev_b32_e32 v130, 16, v153
	v_and_b32_e32 v131, 0xffff0000, v153
	v_mul_f32_e32 v129, 0xbfb8aa3b, v155
	v_pk_fma_f32 v[164:165], v[54:55], v[130:131], v[122:123]
	v_exp_f32_e32 v129, v129
	v_mul_f32_e32 v123, 0xbfb8aa3b, v164
	v_add_f32_e32 v122, 1.0, v128
	v_exp_f32_e32 v123, v123
	v_mul_f32_e32 v128, 0xbfb8aa3b, v165
	v_exp_f32_e32 v128, v128
	v_rcp_f32_e32 v166, v122
	v_add_f32_e32 v122, 1.0, v129
	v_rcp_f32_e32 v167, v122
	v_add_f32_e32 v122, 1.0, v123
	v_rcp_f32_e32 v168, v122
	v_add_f32_e32 v122, 1.0, v128
	v_rcp_f32_e32 v169, v122
	v_pk_fma_f32 v[122:123], v[10:11], v[136:137], 0 op_sel_hi:[1,1,0]
	v_pk_fma_f32 v[128:129], v[8:9], v[134:135], 0 op_sel_hi:[1,1,0]
	v_pk_fma_f32 v[122:123], v[18:19], v[120:121], v[122:123]
	v_pk_fma_f32 v[128:129], v[16:17], v[118:119], v[128:129]
	v_pk_fma_f32 v[122:123], v[30:31], v[102:103], v[122:123]
	v_pk_fma_f32 v[128:129], v[28:29], v[100:101], v[128:129]
	v_pk_fma_f32 v[136:137], v[42:43], v[106:107], v[122:123]
	v_pk_fma_f32 v[134:135], v[40:41], v[104:105], v[128:129]
	v_lshlrev_b32_e32 v122, 16, v152
	v_and_b32_e32 v123, 0xffff0000, v152
	v_pk_fma_f32 v[134:135], v[56:57], v[122:123], v[134:135]
	v_pk_mul_f32 v[156:157], v[156:157], v[160:161]
	v_mul_f32_e32 v152, 0xbfb8aa3b, v135
	v_exp_f32_e32 v170, v152
	v_pk_mul_f32 v[152:153], v[158:159], v[162:163]
	v_mov_b32_e32 v160, v157
	v_mov_b32_e32 v161, v153
	v_mov_b32_e32 v158, v156
	v_mov_b32_e32 v159, v152
	v_pk_mul_f32 v[160:161], v[160:161], v[160:161]
	v_pk_mul_f32 v[154:155], v[154:155], v[166:167]
	v_pk_fma_f32 v[158:159], v[158:159], v[158:159], v[160:161]
	v_pk_mul_f32 v[160:161], v[164:165], v[168:169]
	v_mov_b32_e32 v164, v155
	v_mov_b32_e32 v165, v161
	v_mov_b32_e32 v162, v154
	v_mov_b32_e32 v163, v160
	v_pk_mul_f32 v[164:165], v[164:165], v[164:165]
	v_lshlrev_b32_e32 v128, 16, v151
	v_pk_fma_f32 v[162:163], v[162:163], v[162:163], v[164:165]
	v_mov_b32_e32 v165, v158
	v_mov_b32_e32 v164, v162
	v_mov_b32_e32 v158, v163
	v_pk_add_f32 v[158:159], v[164:165], v[158:159]
	s_nop 1
	v_mov_b32_dpp v163, v159 quad_perm:[1,0,3,2] row_mask:0xf bank_mask:0xf
	s_nop 1
	v_mov_b32_dpp v162, v158 quad_perm:[1,0,3,2] row_mask:0xf bank_mask:0xf
	v_and_b32_e32 v129, 0xffff0000, v151
	v_mul_f32_e32 v151, 0xbfb8aa3b, v134
	v_exp_f32_e32 v151, v151
	v_pk_fma_f32 v[136:137], v[58:59], v[128:129], v[136:137]
	s_waitcnt lgkmcnt(0)
	v_pk_add_f32 v[158:159], v[158:159], v[162:163]
	s_nop 1
	v_mov_b32_dpp v163, v159 quad_perm:[2,3,0,1] row_mask:0xf bank_mask:0xf
	s_nop 1
	v_mov_b32_dpp v162, v158 quad_perm:[2,3,0,1] row_mask:0xf bank_mask:0xf
	v_add_f32_e32 v151, 1.0, v151
	v_rcp_f32_e32 v164, v151
	v_add_f32_e32 v151, 1.0, v170
	v_rcp_f32_e32 v165, v151
	s_waitcnt lgkmcnt(0)
	v_pk_add_f32 v[158:159], v[158:159], v[162:163]
	s_nop 1
	v_mov_b32_dpp v163, v159 row_half_mirror row_mask:0xf bank_mask:0xf
	s_nop 1
	v_mov_b32_dpp v162, v158 row_half_mirror row_mask:0xf bank_mask:0xf
	v_mul_f32_e32 v151, 0xbfb8aa3b, v136
	v_exp_f32_e32 v151, v151
	v_mul_f32_e32 v166, 0xbfb8aa3b, v137
	v_exp_f32_e32 v167, v166
	s_waitcnt lgkmcnt(0)
	v_pk_add_f32 v[158:159], v[158:159], v[162:163]
	s_nop 1
	v_mov_b32_dpp v163, v159 row_mirror row_mask:0xf bank_mask:0xf
	s_nop 1
	v_mov_b32_dpp v162, v158 row_mirror row_mask:0xf bank_mask:0xf
	v_add_f32_e32 v151, 1.0, v151
	v_rcp_f32_e32 v166, v151
	v_add_f32_e32 v151, 1.0, v167
	v_rcp_f32_e32 v167, v151
	s_waitcnt lgkmcnt(0)
	v_pk_add_f32 v[158:159], v[158:159], v[162:163]
	s_lshl_b64 s[12:13], s[72:73], 8
	v_pk_add_f32 v[158:159], v[158:159], s[28:29] op_sel_hi:[1,0]
	v_pk_mul_f32 v[136:137], v[136:137], v[166:167]
	v_mul_f32_e32 v151, 0x4b800000, v159
	v_cmp_gt_f32_e64 s[38:39], s35, v159
	v_cmp_gt_f32_e64 s[40:41], s35, v158
	v_pk_mul_f32 v[134:135], v[134:135], v[164:165]
	v_cndmask_b32_e64 v151, v159, v151, s[38:39]
	v_rsq_f32_e32 v151, v151
	v_lshl_add_u64 v[164:165], s[12:13], 0, v[64:65]
	v_pk_fma_f32 v[108:109], v[0:1], v[108:109], 0 op_sel_hi:[1,1,0]
	v_lshlrev_b64 v[162:163], 1, v[164:165]
	v_mul_f32_e32 v159, 0x45800000, v151
	v_cndmask_b32_e64 v151, v151, v159, s[38:39]
	v_mul_f32_e32 v166, 0x3e000000, v151
	v_mul_f32_e32 v151, 0x4b800000, v158
	v_cndmask_b32_e64 v151, v158, v151, s[40:41]
	v_rsq_f32_e32 v151, v151
	v_pk_mul_f32 v[156:157], v[156:157], v[166:167] op_sel_hi:[1,0]
	v_pk_mul_f32 v[152:153], v[152:153], v[166:167] op_sel_hi:[1,0]
	v_cvt_pk_bf16_f32 v156, v156, v157
	v_cvt_pk_bf16_f32 v157, v152, v153
	v_mul_f32_e32 v152, 0x45800000, v151
	v_cndmask_b32_e64 v152, v151, v152, s[40:41]
	v_pk_fma_f32 v[108:109], v[12:13], v[84:85], v[108:109]
	v_pk_mul_f32 v[154:155], v[154:155], v[152:153] op_sel_hi:[1,0]
	v_pk_mul_f32 v[152:153], v[160:161], v[152:153] op_sel_hi:[1,0]
	v_cvt_pk_bf16_f32 v134, v134, v135
	v_cvt_pk_bf16_f32 v135, v136, v137
	v_lshl_add_u64 v[136:137], s[26:27], 0, v[162:163]
	v_pk_fma_f32 v[108:109], v[20:21], v[88:89], v[108:109]
	v_cvt_pk_bf16_f32 v154, v154, v155
	v_cvt_pk_bf16_f32 v155, v152, v153
	v_lshl_add_u64 v[152:153], s[14:15], 0, v[162:163]
	global_store_dwordx2 v[136:137], v[134:135], off
	v_pk_fma_f32 v[108:109], v[32:33], v[126:127], v[108:109]
	v_lshlrev_b32_e32 v134, 16, v146
	v_and_b32_e32 v135, 0xffff0000, v146
	global_store_dwordx2 v[152:153], v[154:155], off
	v_pk_fma_f32 v[152:153], v[48:49], v[134:135], v[108:109]
	v_pk_fma_f32 v[110:111], v[2:3], v[110:111], 0 op_sel_hi:[1,1,0]
	v_mul_f32_e32 v108, 0xbfb8aa3b, v152
	v_exp_f32_e32 v108, v108
	v_mul_f32_e32 v109, 0xbfb8aa3b, v153
	v_pk_fma_f32 v[110:111], v[14:15], v[86:87], v[110:111]
	v_exp_f32_e32 v109, v109
	v_pk_fma_f32 v[110:111], v[22:23], v[90:91], v[110:111]
	v_lshlrev_b32_e32 v136, 16, v145
	v_pk_fma_f32 v[110:111], v[34:35], v[132:133], v[110:111]
	v_and_b32_e32 v137, 0xffff0000, v145
	v_lshl_add_u64 v[164:165], s[18:19], 0, v[162:163]
	v_pk_fma_f32 v[154:155], v[50:51], v[136:137], v[110:111]
	v_add_f32_e32 v108, 1.0, v108
	global_store_dwordx2 v[164:165], v[156:157], off
	v_rcp_f32_e32 v156, v108
	v_add_f32_e32 v108, 1.0, v109
	v_mul_f32_e32 v109, 0xbfb8aa3b, v154
	v_exp_f32_e32 v109, v109
	v_mul_f32_e32 v110, 0xbfb8aa3b, v155
	v_exp_f32_e32 v110, v110
	v_rcp_f32_e32 v157, v108
	v_add_f32_e32 v108, 1.0, v109
	v_rcp_f32_e32 v158, v108
	v_add_f32_e32 v108, 1.0, v110
	v_pk_fma_f32 v[110:111], v[4:5], v[114:115], 0 op_sel_hi:[1,1,0]
	v_rcp_f32_e32 v159, v108
	v_pk_fma_f32 v[110:111], v[24:25], v[92:93], v[110:111]
	v_pk_fma_f32 v[108:109], v[6:7], v[116:117], 0 op_sel_hi:[1,1,0]
	v_pk_fma_f32 v[110:111], v[44:45], v[96:97], v[110:111]
	v_pk_fma_f32 v[108:109], v[26:27], v[94:95], v[108:109]
	v_pk_fma_f32 v[114:115], v[36:37], v[124:125], v[110:111]
	v_lshlrev_b32_e32 v110, 16, v142
	v_and_b32_e32 v111, 0xffff0000, v142
	v_pk_fma_f32 v[160:161], v[52:53], v[110:111], v[114:115]
	v_pk_fma_f32 v[108:109], v[46:47], v[98:99], v[108:109]
	v_mul_f32_e32 v114, 0xbfb8aa3b, v160
	v_exp_f32_e32 v114, v114
	v_pk_fma_f32 v[108:109], v[38:39], v[130:131], v[108:109]
	v_lshlrev_b32_e32 v116, 16, v141
	v_and_b32_e32 v117, 0xffff0000, v141
	v_mul_f32_e32 v115, 0xbfb8aa3b, v161
	v_pk_fma_f32 v[162:163], v[54:55], v[116:117], v[108:109]
	v_exp_f32_e32 v115, v115
	v_mul_f32_e32 v109, 0xbfb8aa3b, v162
	v_add_f32_e32 v108, 1.0, v114
	v_exp_f32_e32 v109, v109
	v_mul_f32_e32 v114, 0xbfb8aa3b, v163
	v_exp_f32_e32 v114, v114
	v_rcp_f32_e32 v164, v108
	v_add_f32_e32 v108, 1.0, v115
	v_rcp_f32_e32 v165, v108
	v_add_f32_e32 v108, 1.0, v109
	v_pk_fma_f32 v[86:87], v[2:3], v[86:87], 0 op_sel_hi:[1,1,0]
	v_pk_fma_f32 v[84:85], v[0:1], v[84:85], 0 op_sel_hi:[1,1,0]
	v_rcp_f32_e32 v166, v108
	v_add_f32_e32 v108, 1.0, v114
	v_pk_fma_f32 v[84:85], v[12:13], v[88:89], v[84:85]
	v_pk_fma_f32 v[86:87], v[14:15], v[90:91], v[86:87]
	v_rcp_f32_e32 v167, v108
	v_pk_fma_f32 v[108:109], v[10:11], v[120:121], 0 op_sel_hi:[1,1,0]
	v_pk_fma_f32 v[114:115], v[8:9], v[118:119], 0 op_sel_hi:[1,1,0]
	v_pk_fma_f32 v[86:87], v[22:23], v[132:133], v[86:87]
	v_pk_fma_f32 v[84:85], v[20:21], v[126:127], v[84:85]
	v_pk_fma_f32 v[114:115], v[16:17], v[100:101], v[114:115]
	v_pk_fma_f32 v[108:109], v[18:19], v[102:103], v[108:109]
	v_pk_fma_f32 v[84:85], v[32:33], v[134:135], v[84:85]
	v_pk_fma_f32 v[86:87], v[34:35], v[136:137], v[86:87]
	v_lshlrev_b32_e32 v88, 16, v150
	v_and_b32_e32 v89, 0xffff0000, v150
	v_lshlrev_b32_e32 v90, 16, v149
	v_and_b32_e32 v91, 0xffff0000, v149
	v_pk_fma_f32 v[94:95], v[6:7], v[94:95], 0 op_sel_hi:[1,1,0]
	v_pk_fma_f32 v[92:93], v[4:5], v[92:93], 0 op_sel_hi:[1,1,0]
	v_pk_fma_f32 v[108:109], v[30:31], v[106:107], v[108:109]
	v_pk_fma_f32 v[114:115], v[28:29], v[104:105], v[114:115]
	v_pk_fma_f32 v[84:85], v[48:49], v[88:89], v[84:85]
	v_pk_fma_f32 v[86:87], v[50:51], v[90:91], v[86:87]
	v_pk_fma_f32 v[92:93], v[24:25], v[96:97], v[92:93]
	v_pk_fma_f32 v[94:95], v[26:27], v[98:99], v[94:95]
	v_pk_fma_f32 v[118:119], v[40:41], v[122:123], v[114:115]
	v_pk_fma_f32 v[120:121], v[42:43], v[128:129], v[108:109]
	v_lshlrev_b32_e32 v108, 16, v140
	v_and_b32_e32 v109, 0xffff0000, v140
	v_mul_f32_e32 v88, 0xbfb8aa3b, v84
	v_mul_f32_e32 v89, 0xbfb8aa3b, v85
	v_mul_f32_e32 v90, 0xbfb8aa3b, v86
	v_mul_f32_e32 v91, 0xbfb8aa3b, v87
	v_pk_fma_f32 v[94:95], v[46:47], v[130:131], v[94:95]
	v_pk_fma_f32 v[92:93], v[44:45], v[124:125], v[92:93]
	v_pk_fma_f32 v[118:119], v[56:57], v[108:109], v[118:119]
	v_exp_f32_e32 v88, v88
	v_exp_f32_e32 v89, v89
	v_exp_f32_e32 v90, v90
	v_exp_f32_e32 v91, v91
	v_pk_fma_f32 v[92:93], v[36:37], v[110:111], v[92:93]
	v_pk_fma_f32 v[94:95], v[38:39], v[116:117], v[94:95]
	v_lshlrev_b32_e32 v96, 16, v148
	v_and_b32_e32 v97, 0xffff0000, v148
	v_lshlrev_b32_e32 v98, 16, v147
	v_and_b32_e32 v99, 0xffff0000, v147
	v_mul_f32_e32 v140, 0xbfb8aa3b, v119
	v_pk_fma_f32 v[92:93], v[52:53], v[96:97], v[92:93]
	v_pk_fma_f32 v[94:95], v[54:55], v[98:99], v[94:95]
	v_exp_f32_e32 v142, v140
	v_pk_mul_f32 v[140:141], v[154:155], v[158:159]
	v_pk_mul_f32 v[152:153], v[152:153], v[156:157]
	v_mul_f32_e32 v96, 0xbfb8aa3b, v92
	v_mul_f32_e32 v97, 0xbfb8aa3b, v93
	v_mul_f32_e32 v98, 0xbfb8aa3b, v94
	v_mul_f32_e32 v99, 0xbfb8aa3b, v95
	v_mov_b32_e32 v156, v153
	v_mov_b32_e32 v157, v141
	v_exp_f32_e32 v96, v96
	v_exp_f32_e32 v97, v97
	v_exp_f32_e32 v98, v98
	v_exp_f32_e32 v99, v99
	v_mov_b32_e32 v154, v152
	v_mov_b32_e32 v155, v140
	v_pk_mul_f32 v[156:157], v[156:157], v[156:157]
	v_add_f32_e32 v88, 1.0, v88
	v_add_f32_e32 v89, 1.0, v89
	v_add_f32_e32 v90, 1.0, v90
	v_add_f32_e32 v91, 1.0, v91
	v_pk_fma_f32 v[154:155], v[154:155], v[154:155], v[156:157]
	v_pk_mul_f32 v[156:157], v[162:163], v[166:167]
	v_pk_mul_f32 v[158:159], v[160:161], v[164:165]
	v_rcp_f32_e32 v88, v88
	v_rcp_f32_e32 v89, v89
	v_rcp_f32_e32 v90, v90
	v_rcp_f32_e32 v91, v91
	v_mov_b32_e32 v162, v159
	v_mov_b32_e32 v163, v157
	v_mov_b32_e32 v160, v158
	v_mov_b32_e32 v161, v156
	v_pk_mul_f32 v[162:163], v[162:163], v[162:163]
	v_add_f32_e32 v96, 1.0, v96
	v_add_f32_e32 v97, 1.0, v97
	v_add_f32_e32 v98, 1.0, v98
	v_add_f32_e32 v99, 1.0, v99
	v_pk_fma_f32 v[160:161], v[160:161], v[160:161], v[162:163]
	v_rcp_f32_e32 v96, v96
	v_rcp_f32_e32 v97, v97
	v_rcp_f32_e32 v98, v98
	v_rcp_f32_e32 v99, v99
	v_mov_b32_e32 v162, v160
	v_mov_b32_e32 v163, v154
	v_mov_b32_e32 v154, v161
	v_pk_mul_f32 v[86:87], v[86:87], v[90:91]
	v_pk_mul_f32 v[84:85], v[84:85], v[88:89]
	v_pk_add_f32 v[154:155], v[162:163], v[154:155]
	v_mov_b32_e32 v90, v85
	v_mov_b32_e32 v91, v87
	s_nop 1
	v_mov_b32_dpp v161, v155 quad_perm:[1,0,3,2] row_mask:0xf bank_mask:0xf
	s_nop 1
	v_mov_b32_dpp v160, v154 quad_perm:[1,0,3,2] row_mask:0xf bank_mask:0xf
	v_mov_b32_e32 v88, v84
	v_mov_b32_e32 v89, v86
	v_pk_mul_f32 v[90:91], v[90:91], v[90:91]
	v_pk_mul_f32 v[92:93], v[92:93], v[96:97]
	v_pk_fma_f32 v[88:89], v[88:89], v[88:89], v[90:91]
	v_pk_mul_f32 v[90:91], v[94:95], v[98:99]
	v_mov_b32_e32 v96, v93
	v_mov_b32_e32 v97, v91
	v_mov_b32_e32 v94, v92
	v_mov_b32_e32 v95, v90
	v_pk_mul_f32 v[96:97], v[96:97], v[96:97]
	s_waitcnt lgkmcnt(0)
	v_pk_add_f32 v[154:155], v[154:155], v[160:161]
	v_pk_fma_f32 v[94:95], v[94:95], v[94:95], v[96:97]
	v_mov_b32_e32 v97, v88
	v_mov_b32_e32 v96, v94
	v_mov_b32_e32 v88, v95
	s_nop 1
	v_mov_b32_dpp v161, v155 quad_perm:[2,3,0,1] row_mask:0xf bank_mask:0xf
	s_nop 1
	v_mov_b32_dpp v160, v154 quad_perm:[2,3,0,1] row_mask:0xf bank_mask:0xf
	v_pk_add_f32 v[88:89], v[96:97], v[88:89]
	s_nop 1
	v_mov_b32_dpp v95, v89 quad_perm:[1,0,3,2] row_mask:0xf bank_mask:0xf
	s_nop 1
	v_mov_b32_dpp v94, v88 quad_perm:[1,0,3,2] row_mask:0xf bank_mask:0xf
	v_lshlrev_b32_e32 v114, 16, v139
	v_and_b32_e32 v115, 0xffff0000, v139
	v_mul_f32_e32 v139, 0xbfb8aa3b, v118
	s_waitcnt lgkmcnt(0)
	v_pk_add_f32 v[154:155], v[154:155], v[160:161]
	v_exp_f32_e32 v139, v139
	s_nop 1
	v_mov_b32_dpp v161, v155 row_half_mirror row_mask:0xf bank_mask:0xf
	s_nop 1
	v_mov_b32_dpp v160, v154 row_half_mirror row_mask:0xf bank_mask:0xf
	s_waitcnt lgkmcnt(0)
	v_pk_add_f32 v[88:89], v[88:89], v[94:95]
	s_nop 1
	v_mov_b32_dpp v95, v89 quad_perm:[2,3,0,1] row_mask:0xf bank_mask:0xf
	s_nop 1
	v_mov_b32_dpp v94, v88 quad_perm:[2,3,0,1] row_mask:0xf bank_mask:0xf
	v_add_f32_e32 v139, 1.0, v139
	v_pk_fma_f32 v[120:121], v[58:59], v[114:115], v[120:121]
	v_rcp_f32_e32 v162, v139
	v_add_f32_e32 v139, 1.0, v142
	s_waitcnt lgkmcnt(0)
	v_pk_add_f32 v[154:155], v[154:155], v[160:161]
	v_rcp_f32_e32 v163, v139
	v_mul_f32_e32 v139, 0xbfb8aa3b, v120
	s_nop 1
	v_mov_b32_dpp v161, v155 row_mirror row_mask:0xf bank_mask:0xf
	s_nop 1
	v_mov_b32_dpp v160, v154 row_mirror row_mask:0xf bank_mask:0xf
	s_waitcnt lgkmcnt(0)
	v_pk_add_f32 v[88:89], v[88:89], v[94:95]
	v_exp_f32_e32 v139, v139
	v_mul_f32_e32 v142, 0xbfb8aa3b, v121
	s_nop 1
	v_mov_b32_dpp v95, v89 row_half_mirror row_mask:0xf bank_mask:0xf
	s_nop 1
	v_mov_b32_dpp v94, v88 row_half_mirror row_mask:0xf bank_mask:0xf
	v_exp_f32_e32 v142, v142
	v_add_f32_e32 v139, 1.0, v139
	s_waitcnt lgkmcnt(0)
	v_pk_add_f32 v[154:155], v[154:155], v[160:161]
	v_pk_fma_f32 v[102:103], v[10:11], v[102:103], 0 op_sel_hi:[1,1,0]
	v_rcp_f32_e32 v164, v139
	v_add_f32_e32 v139, 1.0, v142
	v_pk_add_f32 v[154:155], v[154:155], s[28:29] op_sel_hi:[1,0]
	v_pk_fma_f32 v[102:103], v[18:19], v[106:107], v[102:103]
	s_waitcnt lgkmcnt(0)
	v_pk_add_f32 v[88:89], v[88:89], v[94:95]
	v_rcp_f32_e32 v165, v139
	v_mul_f32_e32 v139, 0x4b800000, v155
	v_cmp_gt_f32_e64 s[38:39], s35, v155
	v_pk_fma_f32 v[102:103], v[30:31], v[128:129], v[102:103]
	s_nop 1
	v_mov_b32_dpp v95, v89 row_mirror row_mask:0xf bank_mask:0xf
	s_nop 1
	v_mov_b32_dpp v94, v88 row_mirror row_mask:0xf bank_mask:0xf
	v_cndmask_b32_e64 v139, v155, v139, s[38:39]
	v_pk_fma_f32 v[102:103], v[42:43], v[114:115], v[102:103]
	v_lshlrev_b32_e32 v106, 16, v143
	v_and_b32_e32 v107, 0xffff0000, v143
	v_rsq_f32_e32 v139, v139
	v_pk_fma_f32 v[102:103], v[58:59], v[106:107], v[102:103]
	v_pk_fma_f32 v[100:101], v[8:9], v[100:101], 0 op_sel_hi:[1,1,0]
	v_mul_f32_e32 v98, 0xbfb8aa3b, v102
	v_mul_f32_e32 v99, 0xbfb8aa3b, v103
	v_exp_f32_e32 v98, v98
	v_exp_f32_e32 v99, v99
	s_waitcnt lgkmcnt(0)
	v_pk_add_f32 v[88:89], v[88:89], v[94:95]
	v_mul_f32_e32 v142, 0x45800000, v139
	v_pk_fma_f32 v[100:101], v[16:17], v[104:105], v[100:101]
	v_pk_add_f32 v[88:89], v[88:89], s[28:29] op_sel_hi:[1,0]
	v_cndmask_b32_e64 v139, v139, v142, s[38:39]
	v_pk_fma_f32 v[100:101], v[28:29], v[122:123], v[100:101]
	v_mul_f32_e32 v94, 0x4b800000, v89
	v_cmp_gt_f32_e64 s[38:39], s35, v89
	v_pk_fma_f32 v[100:101], v[40:41], v[108:109], v[100:101]
	v_lshlrev_b32_e32 v104, 16, v144
	v_and_b32_e32 v105, 0xffff0000, v144
	v_add_f32_e32 v98, 1.0, v98
	v_add_f32_e32 v99, 1.0, v99
	v_cndmask_b32_e64 v89, v89, v94, s[38:39]
	v_pk_fma_f32 v[100:101], v[56:57], v[104:105], v[100:101]
	v_rcp_f32_e32 v98, v98
	v_rcp_f32_e32 v99, v99
	v_rsq_f32_e32 v89, v89
	v_cmp_gt_f32_e64 s[40:41], s35, v154
	v_mul_f32_e32 v142, 0x3e000000, v139
	v_mul_f32_e32 v139, 0x4b800000, v154
	v_mul_f32_e32 v104, 0xbfb8aa3b, v100
	v_mul_f32_e32 v105, 0xbfb8aa3b, v101
	v_cndmask_b32_e64 v139, v154, v139, s[40:41]
	v_exp_f32_e32 v104, v104
	v_exp_f32_e32 v105, v105
	v_rsq_f32_e32 v139, v139
	v_pk_mul_f32 v[98:99], v[102:103], v[98:99]
	v_mul_f32_e32 v102, 0x45800000, v89
	v_cndmask_b32_e64 v89, v89, v102, s[38:39]
	v_pk_mul_f32 v[152:153], v[152:153], v[142:143] op_sel_hi:[1,0]
	v_pk_mul_f32 v[140:141], v[140:141], v[142:143] op_sel_hi:[1,0]
	v_add_f32_e32 v96, 1.0, v104
	v_add_f32_e32 v97, 1.0, v105
	v_mul_f32_e32 v102, 0x3e000000, v89
	v_cvt_pk_bf16_f32 v152, v152, v153
	v_cvt_pk_bf16_f32 v153, v140, v141
	v_mul_f32_e32 v140, 0x45800000, v139
	v_rcp_f32_e32 v96, v96
	v_rcp_f32_e32 v97, v97
	v_pk_mul_f32 v[84:85], v[84:85], v[102:103] op_sel_hi:[1,0]
	s_lshl_b64 s[12:13], s[64:65], 8
	v_cndmask_b32_e64 v140, v139, v140, s[40:41]
	v_cmp_gt_f32_e64 s[40:41], s35, v88
	v_cvt_pk_bf16_f32 v84, v84, v85
	v_mul_f32_e32 v85, 0x4b800000, v88
	v_pk_mul_f32 v[118:119], v[118:119], v[162:163]
	v_lshl_add_u64 v[162:163], s[12:13], 0, v[64:65]
	v_cndmask_b32_e64 v85, v88, v85, s[40:41]
	v_lshlrev_b64 v[160:161], 1, v[162:163]
	s_lshl_b64 s[12:13], s[6:7], 8
	v_rsq_f32_e32 v88, v85
	v_lshl_add_u64 v[162:163], s[18:19], 0, v[160:161]
	v_pk_mul_f32 v[96:97], v[100:101], v[96:97]
	v_lshl_add_u64 v[100:101], s[12:13], 0, v[64:65]
	v_pk_mul_f32 v[120:121], v[120:121], v[164:165]
	global_store_dwordx2 v[162:163], v[152:153], off
	v_pk_mul_f32 v[152:153], v[158:159], v[140:141] op_sel_hi:[1,0]
	v_pk_mul_f32 v[140:141], v[156:157], v[140:141] op_sel_hi:[1,0]
	v_lshlrev_b64 v[94:95], 1, v[100:101]
	v_pk_mul_f32 v[86:87], v[86:87], v[102:103] op_sel_hi:[1,0]
	v_cvt_pk_bf16_f32 v152, v152, v153
	v_cvt_pk_bf16_f32 v153, v140, v141
	v_lshl_add_u64 v[140:141], s[14:15], 0, v[160:161]
	v_cvt_pk_bf16_f32 v118, v118, v119
	v_cvt_pk_bf16_f32 v119, v120, v121
	v_lshl_add_u64 v[120:121], s[26:27], 0, v[160:161]
	v_lshl_add_u64 v[100:101], s[18:19], 0, v[94:95]
	v_cvt_pk_bf16_f32 v85, v86, v87
	global_store_dwordx2 v[140:141], v[152:153], off
	global_store_dwordx2 v[120:121], v[118:119], off
	global_store_dwordx2 v[100:101], v[84:85], off
	v_mul_f32_e32 v84, 0x45800000, v88
	v_cndmask_b32_e64 v84, v88, v84, s[40:41]
	v_pk_mul_f32 v[86:87], v[92:93], v[84:85] op_sel_hi:[1,0]
	v_pk_mul_f32 v[84:85], v[90:91], v[84:85] op_sel_hi:[1,0]
	v_cvt_pk_bf16_f32 v86, v86, v87
	v_cvt_pk_bf16_f32 v87, v84, v85
	v_lshl_add_u64 v[84:85], s[14:15], 0, v[94:95]
	global_store_dwordx2 v[84:85], v[86:87], off
	v_cvt_pk_bf16_f32 v84, v96, v97
	v_cvt_pk_bf16_f32 v85, v98, v99
	v_lshl_add_u64 v[86:87], s[26:27], 0, v[94:95]
	global_store_dwordx2 v[86:87], v[84:85], off
	s_and_saveexec_b64 s[12:13], vcc
	s_xor_b64 s[38:39], exec, s[12:13]
	s_cbranch_execz .LBB0_345
	v_mul_f32_e32 v84, 0xbfb8aa3b, v112
	v_exp_f32_e32 v84, v84
	s_nop 0
	v_add_f32_e32 v84, 1.0, v84
	v_rcp_f32_e32 v84, v84

.LBB0_922:
	s_add_i32 s26, s4, s2
	s_ashr_i32 s6, s26, 12
	s_mulk_i32 s6, 0x1100
	s_add_i32 s27, s6, 0x100
	s_and_b32 s6, s26, 0xffc
	v_readlane_b32 vcc_lo, v252, 6
	s_add_i32 s28, s27, s6
	v_readlane_b32 vcc_hi, v252, 7
	s_and_b64 s[6:7], vcc, exec
	s_cselect_b32 s70, s26, s28
	s_mul_hi_i32 s6, s70, 0x78787879
	s_lshr_b32 s7, s6, 31
	s_ashr_i32 s6, s6, 11
	s_add_i32 s6, s6, s7
	s_mul_i32 s7, s6, 0xffffef00
	s_add_i32 s7, s7, s70
	s_cmpk_gt_i32 s7, 0xff
	s_cselect_b32 s33, s6, 16
	s_ashr_i32 s71, s70, 31
	s_lshl_b64 s[64:65], s[70:71], 11
	v_lshl_add_u64 v[32:33], v[58:59], 0, s[64:65]
	global_load_dwordx4 v[70:73], v[32:33], off
	global_load_dwordx4 v[74:77], v[32:33], off offset:1024
	s_add_i32 s28, s26, 1
	s_and_b32 s6, s28, 0xffd
	s_add_i32 s29, s27, s6
	s_and_b64 s[6:7], vcc, exec
	s_cselect_b32 s48, s28, s29
	s_add_i32 s28, s26, 2
	s_ashr_i32 s49, s48, 31
	s_and_b32 s6, s28, 0xffe
	s_lshl_b64 s[46:47], s[48:49], 11
	s_add_i32 s29, s27, s6
	s_and_b64 s[6:7], vcc, exec
	s_cselect_b32 s42, s28, s29
	s_add_i32 s26, s26, 3
	s_ashr_i32 s43, s42, 31
	s_and_b32 s6, s26, 0xfff
	s_lshl_b64 s[40:41], s[42:43], 11
	s_add_i32 s27, s27, s6
	s_and_b64 s[6:7], vcc, exec
	s_cselect_b32 s26, s26, s27
	v_lshl_add_u64 v[32:33], v[58:59], 0, s[46:47]
	s_ashr_i32 s27, s26, 31
	global_load_dwordx4 v[52:55], v[32:33], off
	global_load_dwordx4 v[48:51], v[32:33], off offset:1024
	v_lshl_add_u64 v[32:33], v[58:59], 0, s[40:41]
	s_lshl_b64 s[6:7], s[26:27], 11
	global_load_dwordx4 v[44:47], v[32:33], off
	global_load_dwordx4 v[40:43], v[32:33], off offset:1024
	v_lshl_add_u64 v[32:33], v[58:59], 0, s[6:7]
	global_load_dwordx4 v[36:39], v[32:33], off
	s_nop 0
	global_load_dwordx4 v[32:35], v[32:33], off offset:1024
	s_cmp_eq_u32 s33, s14
	s_waitcnt vmcnt(7)
	v_and_b32_e32 v97, 0xffff0000, v70
	v_and_b32_e32 v93, 0xffff0000, v71
	v_lshlrev_b32_e32 v96, 16, v70
	v_lshlrev_b32_e32 v92, 16, v71
	v_mul_f32_e32 v70, v97, v97
	v_mul_f32_e32 v71, v93, v93
	v_and_b32_e32 v89, 0xffff0000, v72
	v_and_b32_e32 v87, 0xffff0000, v73
	v_fmac_f32_e32 v70, v96, v96
	v_fmac_f32_e32 v71, v92, v92
	v_lshlrev_b32_e32 v88, 16, v72
	v_lshlrev_b32_e32 v86, 16, v73
	v_add_f32_e32 v70, v70, v71
	v_mul_f32_e32 v71, v89, v89
	v_mul_f32_e32 v72, v87, v87
	v_fmac_f32_e32 v71, v88, v88
	v_fmac_f32_e32 v72, v86, v86
	v_add_f32_e32 v71, v71, v72
	s_waitcnt vmcnt(6)
	v_and_b32_e32 v83, 0xffff0000, v74
	v_and_b32_e32 v85, 0xffff0000, v75
	v_add_f32_e32 v70, v70, v71
	v_lshlrev_b32_e32 v82, 16, v74
	v_lshlrev_b32_e32 v84, 16, v75
	v_mul_f32_e32 v71, v83, v83
	v_mul_f32_e32 v72, v85, v85
	v_and_b32_e32 v79, 0xffff0000, v76
	v_and_b32_e32 v81, 0xffff0000, v77
	v_fmac_f32_e32 v71, v82, v82
	v_fmac_f32_e32 v72, v84, v84
	v_lshlrev_b32_e32 v78, 16, v76
	v_lshlrev_b32_e32 v80, 16, v77
	v_add_f32_e32 v71, v71, v72
	v_mul_f32_e32 v72, v79, v79
	v_mul_f32_e32 v73, v81, v81
	v_fmac_f32_e32 v72, v78, v78
	v_fmac_f32_e32 v73, v80, v80
	v_add_f32_e32 v72, v72, v73
	v_add_f32_e32 v71, v71, v72
	v_add_f32_e32 v70, v70, v71
	s_nop 1
	v_mov_b32_dpp v71, v70 quad_perm:[1,0,3,2] row_mask:0xf bank_mask:0xf
	s_waitcnt lgkmcnt(0)
	v_add_f32_e32 v70, v70, v71
	s_nop 1
	v_mov_b32_dpp v71, v70 quad_perm:[2,3,0,1] row_mask:0xf bank_mask:0xf
	s_waitcnt lgkmcnt(0)
	v_add_f32_e32 v70, v70, v71
	s_nop 1
	v_mov_b32_dpp v71, v70 row_half_mirror row_mask:0xf bank_mask:0xf
	s_waitcnt lgkmcnt(0)
	v_add_f32_e32 v70, v70, v71
	s_nop 1
	v_mov_b32_dpp v71, v70 row_mirror row_mask:0xf bank_mask:0xf
	s_waitcnt lgkmcnt(0)
	v_add_f32_e32 v70, v70, v71
	v_mov_b32_e32 v71, v70
	s_nop 1
	v_permlane16_swap_b32_e32 v70, v71
	s_waitcnt lgkmcnt(0)
	v_add_f32_e32 v104, v70, v71
	v_mov_b32_e32 v105, v104
	s_nop 1
	v_permlane32_swap_b32_e32 v104, v105
	s_cbranch_scc1 .LBB0_924
	s_add_i32 s14, s33, s13
	s_mul_hi_i32 s29, s14, 0x6000
	s_mulk_i32 s14, 0x6000
	s_add_u32 s28, s60, s14
	s_addc_u32 s29, s63, s29
	v_lshl_add_u64 v[16:17], v[56:57], 2, s[28:29]
	v_add_co_u32_e32 v8, vcc, 0x4000, v16
	s_mov_b64 s[28:29], 0x4000
	s_nop 0
	v_addc_co_u32_e32 v9, vcc, 0, v17, vcc
	global_load_dwordx4 v[4:7], v[60:61], off offset:16
	global_load_dwordx4 v[0:3], v[60:61], off
	v_lshl_add_u64 v[28:29], v[16:17], 0, s[28:29]
	global_load_dwordx4 v[8:11], v[8:9], off
	s_nop 0
	global_load_dwordx4 v[12:15], v[28:29], off offset:16
	s_movk_i32 s14, 0x3000
	s_mov_b64 s[28:29], 0x3000
	v_lshl_add_u64 v[70:71], v[16:17], 0, s[28:29]
	s_waitcnt vmcnt(1)
	v_pk_add_f32 v[8:9], v[8:9], 1.0 op_sel_hi:[1,0]
	s_nop 0
	v_pk_mul_f32 v[0:1], v[0:1], v[8:9]
	s_waitcnt vmcnt(0)
	v_pk_add_f32 v[8:9], v[14:15], 1.0 op_sel_hi:[1,0]
	v_pk_add_f32 v[10:11], v[10:11], 1.0 op_sel_hi:[1,0]
	v_pk_mul_f32 v[6:7], v[6:7], v[8:9]
	v_add_co_u32_e32 v8, vcc, s14, v16
	v_pk_mul_f32 v[2:3], v[2:3], v[10:11]
	v_pk_add_f32 v[10:11], v[12:13], 1.0 op_sel_hi:[1,0]
	v_addc_co_u32_e32 v9, vcc, 0, v17, vcc
	v_pk_mul_f32 v[4:5], v[4:5], v[10:11]
	global_load_dwordx4 v[8:11], v[8:9], off
	s_nop 0
	global_load_dwordx4 v[12:15], v[70:71], off offset:16
	global_load_dwordx4 v[20:23], v[60:61], off offset:2064
	global_load_dwordx4 v[16:19], v[60:61], off offset:2048
	global_load_dwordx4 v[24:27], v[28:29], off offset:2064
	s_nop 0
	global_load_dwordx4 v[28:31], v[28:29], off offset:2048
	s_mov_b32 s14, s33
	s_waitcnt vmcnt(1)
	v_pk_add_f32 v[26:27], v[26:27], 1.0 op_sel_hi:[1,0]
	s_waitcnt vmcnt(0)
	v_pk_add_f32 v[30:31], v[30:31], 1.0 op_sel_hi:[1,0]
	v_pk_add_f32 v[28:29], v[28:29], 1.0 op_sel_hi:[1,0]
	v_pk_add_f32 v[24:25], v[24:25], 1.0 op_sel_hi:[1,0]
	v_pk_mul_f32 v[18:19], v[18:19], v[30:31]
	v_pk_mul_f32 v[16:17], v[16:17], v[28:29]
	v_pk_mul_f32 v[22:23], v[22:23], v[26:27]
	v_pk_mul_f32 v[20:21], v[20:21], v[24:25]
	global_load_dwordx4 v[24:27], v[70:71], off offset:2064
	global_load_dwordx4 v[28:31], v[70:71], off offset:2048

.LBB0_926:
	v_add_f32_e32 v48, v48, v49
	v_fmamk_f32 v48, v48, 0x3a800000, v196
	v_cmp_gt_f32_e32 vcc, s35, v48
	v_mul_f32_e32 v49, 0x4b800000, v48
	v_and_b32_e32 v55, 0xffff0000, v44
	v_cndmask_b32_e32 v48, v48, v49, vcc
	v_rsq_f32_e32 v48, v48
	v_and_b32_e32 v53, 0xffff0000, v45
	v_lshlrev_b32_e32 v54, 16, v44
	v_lshlrev_b32_e32 v52, 16, v45
	v_mul_f32_e32 v49, 0x45800000, v48
	v_mul_f32_e32 v44, v55, v55
	v_mul_f32_e32 v45, v53, v53
	v_cndmask_b32_e32 v82, v48, v49, vcc
	v_and_b32_e32 v51, 0xffff0000, v46
	v_and_b32_e32 v49, 0xffff0000, v47
	v_fmac_f32_e32 v44, v54, v54
	v_fmac_f32_e32 v45, v52, v52
	v_lshlrev_b32_e32 v50, 16, v46
	v_lshlrev_b32_e32 v48, 16, v47
	v_add_f32_e32 v44, v44, v45
	v_mul_f32_e32 v45, v51, v51
	v_mul_f32_e32 v46, v49, v49
	v_fmac_f32_e32 v45, v50, v50
	v_fmac_f32_e32 v46, v48, v48
	v_add_f32_e32 v45, v45, v46
	v_add_f32_e32 v78, v44, v45
	v_and_b32_e32 v45, 0xffff0000, v40
	v_and_b32_e32 v47, 0xffff0000, v41
	v_lshlrev_b32_e32 v44, 16, v40
	v_lshlrev_b32_e32 v46, 16, v41
	v_mul_f32_e32 v79, v45, v45
	v_mul_f32_e32 v80, v47, v47
	v_lshlrev_b32_e32 v40, 16, v42
	v_and_b32_e32 v41, 0xffff0000, v42
	v_lshlrev_b32_e32 v42, 16, v43
	v_and_b32_e32 v43, 0xffff0000, v43
	v_fmac_f32_e32 v79, v44, v44
	v_fmac_f32_e32 v80, v46, v46
	v_add_f32_e32 v79, v79, v80
	v_mul_f32_e32 v80, v41, v41
	v_mul_f32_e32 v81, v43, v43
	v_fmac_f32_e32 v80, v40, v40
	v_fmac_f32_e32 v81, v42, v42
	v_add_f32_e32 v80, v80, v81
	v_add_f32_e32 v79, v79, v80
	v_add_f32_e32 v96, v78, v79
	v_pk_mul_f32 v[78:79], v[82:83], v[100:101] op_sel_hi:[0,1]
	v_pk_mul_f32 v[80:81], v[82:83], v[98:99] op_sel_hi:[0,1]
	v_pk_fma_f32 v[84:85], v[80:81], v[2:3], v[10:11]
	v_pk_fma_f32 v[86:87], v[78:79], v[0:1], v[8:9]
	v_pk_mul_f32 v[78:79], v[82:83], v[94:95] op_sel_hi:[0,1]
	v_pk_mul_f32 v[80:81], v[82:83], v[90:91] op_sel_hi:[0,1]
	v_pk_fma_f32 v[88:89], v[80:81], v[6:7], v[14:15]
	v_pk_fma_f32 v[90:91], v[78:79], v[4:5], v[12:13]
	v_cvt_pk_bf16_f32 v78, v86, v87
	v_cvt_pk_bf16_f32 v79, v84, v85
	v_cvt_pk_bf16_f32 v80, v90, v91
	v_cvt_pk_bf16_f32 v81, v88, v89
	v_lshl_add_u64 v[92:93], v[62:63], 0, s[46:47]
	global_store_dwordx4 v[92:93], v[78:81], off
	s_mul_hi_i32 s14, s42, 0x78787879
	s_lshr_b32 s28, s14, 31
	v_mov_b32_e32 v78, v113
	v_mov_b32_e32 v79, v113
	v_cvt_pk_fp8_f32 v78, v86, v87
	v_cvt_pk_fp8_f32 v79, v90, v91
	s_ashr_i32 s14, s14, 11
	s_add_i32 s14, s14, s28
	s_mul_i32 s28, s14, 0xffffef00
	s_add_i32 s28, s28, s42
	v_cvt_pk_fp8_f32 v78, v84, v85 op_sel:[0,0,1]
	v_cvt_pk_fp8_f32 v79, v88, v89 op_sel:[0,0,1]
	s_cmpk_gt_i32 s28, 0xff
	s_cselect_b32 s14, s14, 16
	s_lshl_b64 s[28:29], s[48:49], 10
	v_lshl_add_u64 v[80:81], v[68:69], 0, s[28:29]
	v_pk_mul_f32 v[72:73], v[82:83], v[72:73] op_sel_hi:[0,1]
	global_store_dwordx2 v[80:81], v[78:79], off
	v_pk_mul_f32 v[76:77], v[82:83], v[76:77] op_sel_hi:[0,1]
	s_waitcnt vmcnt(2)
	v_pk_fma_f32 v[78:79], v[72:73], v[16:17], v[28:29]
	v_pk_mul_f32 v[70:71], v[82:83], v[70:71] op_sel_hi:[0,1]
	v_pk_mul_f32 v[72:73], v[82:83], v[74:75] op_sel_hi:[0,1]
	v_pk_fma_f32 v[76:77], v[76:77], v[18:19], v[30:31]
	v_pk_fma_f32 v[74:75], v[72:73], v[22:23], v[26:27]
	v_pk_fma_f32 v[82:83], v[70:71], v[20:21], v[24:25]
	v_cvt_pk_bf16_f32 v70, v78, v79
	v_cvt_pk_bf16_f32 v71, v76, v77
	v_cvt_pk_bf16_f32 v72, v82, v83
	v_cvt_pk_bf16_f32 v73, v74, v75
	global_store_dwordx4 v[92:93], v[70:73], off offset:1024
	s_cmp_eq_u32 s14, s33
	s_mov_b64 s[64:65], 0xc00
	v_mov_b32_e32 v70, v113
	v_mov_b32_e32 v71, v113
	v_cvt_pk_fp8_f32 v70, v78, v79
	v_cvt_pk_fp8_f32 v71, v82, v83
	v_readlane_b32 s70, v255, 14
	s_mov_b32 s21, s20
	v_cvt_pk_fp8_f32 v70, v76, v77 op_sel:[0,0,1]
	v_cvt_pk_fp8_f32 v71, v74, v75 op_sel:[0,0,1]
	s_mov_b32 s71, s66
	global_store_dwordx2 v[80:81], v[70:71], off offset:512
	s_nop 1
	v_mov_b32_dpp v70, v96 quad_perm:[1,0,3,2] row_mask:0xf bank_mask:0xf
	s_waitcnt lgkmcnt(0)
	v_add_f32_e32 v70, v96, v70
	s_nop 1
	v_mov_b32_dpp v71, v70 quad_perm:[2,3,0,1] row_mask:0xf bank_mask:0xf
	s_waitcnt lgkmcnt(0)
	v_add_f32_e32 v70, v70, v71
	s_nop 1
	v_mov_b32_dpp v71, v70 row_half_mirror row_mask:0xf bank_mask:0xf
	s_waitcnt lgkmcnt(0)
	v_add_f32_e32 v70, v70, v71
	s_nop 1
	v_mov_b32_dpp v71, v70 row_mirror row_mask:0xf bank_mask:0xf
	s_waitcnt lgkmcnt(0)
	v_add_f32_e32 v70, v70, v71
	v_mov_b32_e32 v71, v70
	s_nop 1
	v_permlane16_swap_b32_e32 v70, v71
	s_waitcnt lgkmcnt(0)
	v_add_f32_e32 v70, v70, v71
	v_mov_b32_e32 v71, v70
	s_nop 1
	v_permlane32_swap_b32_e32 v70, v71
	s_cbranch_scc1 .LBB0_928
	s_add_i32 s28, s14, s13
	s_mul_hi_i32 s29, s28, 0x6000
	s_mulk_i32 s28, 0x6000
	s_add_u32 s28, s60, s28
	s_addc_u32 s29, s63, s29
	v_lshl_add_u64 v[16:17], v[56:57], 2, s[28:29]
	v_add_co_u32_e32 v8, vcc, 0x4000, v16
	s_mov_b64 s[28:29], 0x4000
	s_nop 0
	v_addc_co_u32_e32 v9, vcc, 0, v17, vcc
	global_load_dwordx4 v[4:7], v[60:61], off offset:16
	global_load_dwordx4 v[0:3], v[60:61], off
	v_lshl_add_u64 v[28:29], v[16:17], 0, s[28:29]
	global_load_dwordx4 v[8:11], v[8:9], off
	s_nop 0
	global_load_dwordx4 v[12:15], v[28:29], off offset:16
	s_mov_b64 s[28:29], 0x3000
	v_lshl_add_u64 v[72:73], v[16:17], 0, s[28:29]
	s_movk_i32 s28, 0x3000
	s_mov_b32 s33, s14
	s_waitcnt vmcnt(1)
	v_pk_add_f32 v[8:9], v[8:9], 1.0 op_sel_hi:[1,0]
	s_nop 0
	v_pk_mul_f32 v[0:1], v[0:1], v[8:9]
	s_waitcnt vmcnt(0)
	v_pk_add_f32 v[8:9], v[14:15], 1.0 op_sel_hi:[1,0]
	v_pk_add_f32 v[10:11], v[10:11], 1.0 op_sel_hi:[1,0]
	v_pk_mul_f32 v[6:7], v[6:7], v[8:9]
	v_add_co_u32_e32 v8, vcc, s28, v16
	v_pk_mul_f32 v[2:3], v[2:3], v[10:11]
	v_pk_add_f32 v[10:11], v[12:13], 1.0 op_sel_hi:[1,0]
	v_addc_co_u32_e32 v9, vcc, 0, v17, vcc
	v_pk_mul_f32 v[4:5], v[4:5], v[10:11]
	global_load_dwordx4 v[8:11], v[8:9], off
	s_nop 0
	global_load_dwordx4 v[12:15], v[72:73], off offset:16
	global_load_dwordx4 v[20:23], v[60:61], off offset:2064
	global_load_dwordx4 v[16:19], v[60:61], off offset:2048
	global_load_dwordx4 v[24:27], v[28:29], off offset:2064
	s_nop 0
	global_load_dwordx4 v[28:31], v[28:29], off offset:2048
	s_waitcnt vmcnt(1)
	v_pk_add_f32 v[26:27], v[26:27], 1.0 op_sel_hi:[1,0]
	s_waitcnt vmcnt(0)
	v_pk_add_f32 v[30:31], v[30:31], 1.0 op_sel_hi:[1,0]
	v_pk_add_f32 v[28:29], v[28:29], 1.0 op_sel_hi:[1,0]
	v_pk_add_f32 v[24:25], v[24:25], 1.0 op_sel_hi:[1,0]
	v_pk_mul_f32 v[18:19], v[18:19], v[30:31]
	v_pk_mul_f32 v[16:17], v[16:17], v[28:29]
	v_pk_mul_f32 v[22:23], v[22:23], v[26:27]
	v_pk_mul_f32 v[20:21], v[20:21], v[24:25]
	global_load_dwordx4 v[24:27], v[72:73], off offset:2064
	global_load_dwordx4 v[28:31], v[72:73], off offset:2048
.LBB0_928:
	v_add_f32_e32 v70, v70, v71
	v_fmamk_f32 v70, v70, 0x3a800000, v196
	v_cmp_gt_f32_e32 vcc, s35, v70
	v_mul_f32_e32 v71, 0x4b800000, v70
	v_and_b32_e32 v79, 0xffff0000, v36
	v_cndmask_b32_e32 v70, v70, v71, vcc
	v_rsq_f32_e32 v70, v70
	v_and_b32_e32 v77, 0xffff0000, v37
	v_lshlrev_b32_e32 v78, 16, v36
	v_lshlrev_b32_e32 v76, 16, v37
	v_mul_f32_e32 v36, v79, v79
	v_mul_f32_e32 v37, v77, v77
	v_and_b32_e32 v75, 0xffff0000, v38
	v_and_b32_e32 v73, 0xffff0000, v39
	v_fmac_f32_e32 v36, v78, v78
	v_fmac_f32_e32 v37, v76, v76
	v_lshlrev_b32_e32 v74, 16, v38
	v_lshlrev_b32_e32 v72, 16, v39
	v_add_f32_e32 v36, v36, v37
	v_mul_f32_e32 v37, v75, v75
	v_mul_f32_e32 v38, v73, v73
	v_mul_f32_e32 v71, 0x45800000, v70
	v_fmac_f32_e32 v37, v74, v74
	v_fmac_f32_e32 v38, v72, v72
	v_cndmask_b32_e32 v80, v70, v71, vcc
	v_add_f32_e32 v37, v37, v38
	v_and_b32_e32 v71, 0xffff0000, v32
	v_and_b32_e32 v39, 0xffff0000, v33
	v_add_f32_e32 v81, v36, v37
	v_lshlrev_b32_e32 v70, 16, v32
	v_lshlrev_b32_e32 v38, 16, v33
	v_lshlrev_b32_e32 v36, 16, v34
	v_and_b32_e32 v37, 0xffff0000, v34
	v_lshlrev_b32_e32 v32, 16, v35
	v_and_b32_e32 v33, 0xffff0000, v35
	v_mul_f32_e32 v34, v71, v71
	v_mul_f32_e32 v35, v39, v39
	v_fmac_f32_e32 v34, v70, v70
	v_fmac_f32_e32 v35, v38, v38
	v_add_f32_e32 v34, v34, v35
	v_mul_f32_e32 v35, v37, v37
	v_mul_f32_e32 v82, v33, v33
	v_fmac_f32_e32 v35, v36, v36
	v_fmac_f32_e32 v82, v32, v32
	v_add_f32_e32 v35, v35, v82
	v_add_f32_e32 v34, v34, v35
	v_add_f32_e32 v81, v81, v34
	v_pk_mul_f32 v[34:35], v[80:81], v[54:55] op_sel_hi:[0,1]
	v_pk_mul_f32 v[52:53], v[80:81], v[52:53] op_sel_hi:[0,1]
	v_pk_mul_f32 v[50:51], v[80:81], v[50:51] op_sel_hi:[0,1]
	v_pk_mul_f32 v[48:49], v[80:81], v[48:49] op_sel_hi:[0,1]
	v_pk_fma_f32 v[52:53], v[52:53], v[2:3], v[10:11]
	v_pk_fma_f32 v[34:35], v[34:35], v[0:1], v[8:9]
	v_pk_fma_f32 v[54:55], v[48:49], v[6:7], v[14:15]
	v_pk_fma_f32 v[82:83], v[50:51], v[4:5], v[12:13]
	v_cvt_pk_bf16_f32 v48, v34, v35
	v_cvt_pk_bf16_f32 v49, v52, v53
	v_cvt_pk_bf16_f32 v50, v82, v83
	v_cvt_pk_bf16_f32 v51, v54, v55
	v_lshl_add_u64 v[84:85], v[62:63], 0, s[40:41]
	global_store_dwordx4 v[84:85], v[48:51], off
	s_mul_hi_i32 s14, s26, 0x78787879
	s_lshr_b32 s28, s14, 31
	v_mov_b32_e32 v48, v113
	v_mov_b32_e32 v49, v113
	v_cvt_pk_fp8_f32 v48, v34, v35
	v_cvt_pk_fp8_f32 v49, v82, v83
	s_ashr_i32 s14, s14, 11
	s_add_i32 s14, s14, s28
	s_mul_i32 s28, s14, 0xffffef00
	s_add_i32 s28, s28, s26
	v_cvt_pk_fp8_f32 v48, v52, v53 op_sel:[0,0,1]
	v_cvt_pk_fp8_f32 v49, v54, v55 op_sel:[0,0,1]
	s_cmpk_gt_i32 s28, 0xff
	s_cselect_b32 s14, s14, 16
	s_lshl_b64 s[28:29], s[42:43], 10
	v_lshl_add_u64 v[34:35], v[68:69], 0, s[28:29]
	v_pk_mul_f32 v[44:45], v[80:81], v[44:45] op_sel_hi:[0,1]
	v_pk_mul_f32 v[46:47], v[80:81], v[46:47] op_sel_hi:[0,1]
	v_pk_mul_f32 v[40:41], v[80:81], v[40:41] op_sel_hi:[0,1]
	v_pk_mul_f32 v[42:43], v[80:81], v[42:43] op_sel_hi:[0,1]
	global_store_dwordx2 v[34:35], v[48:49], off
	s_waitcnt vmcnt(2)
	v_pk_fma_f32 v[46:47], v[46:47], v[18:19], v[30:31]
	v_pk_fma_f32 v[44:45], v[44:45], v[16:17], v[28:29]
	v_pk_fma_f32 v[48:49], v[42:43], v[22:23], v[26:27]
	v_pk_fma_f32 v[50:51], v[40:41], v[20:21], v[24:25]
	v_cvt_pk_bf16_f32 v40, v44, v45
	v_cvt_pk_bf16_f32 v41, v46, v47
	v_cvt_pk_bf16_f32 v42, v50, v51
	v_cvt_pk_bf16_f32 v43, v48, v49
	global_store_dwordx4 v[84:85], v[40:43], off offset:1024
	s_cmp_eq_u32 s14, s33
	s_mov_b64 s[48:49], 0x80000
	v_mov_b32_e32 v40, v113
	v_mov_b32_e32 v41, v113
	v_cvt_pk_fp8_f32 v40, v44, v45
	v_cvt_pk_fp8_f32 v41, v50, v51
	v_cvt_pk_fp8_f32 v40, v46, v47 op_sel:[0,0,1]
	v_cvt_pk_fp8_f32 v41, v48, v49 op_sel:[0,0,1]
	global_store_dwordx2 v[34:35], v[40:41], off offset:512
	s_nop 1
	v_mov_b32_dpp v34, v81 quad_perm:[1,0,3,2] row_mask:0xf bank_mask:0xf
	s_waitcnt lgkmcnt(0)
	v_add_f32_e32 v34, v81, v34
	s_nop 1
	v_mov_b32_dpp v35, v34 quad_perm:[2,3,0,1] row_mask:0xf bank_mask:0xf
	s_waitcnt lgkmcnt(0)
	v_add_f32_e32 v34, v34, v35
	s_nop 1
	v_mov_b32_dpp v35, v34 row_half_mirror row_mask:0xf bank_mask:0xf
	s_waitcnt lgkmcnt(0)
	v_add_f32_e32 v34, v34, v35
	s_nop 1
	v_mov_b32_dpp v35, v34 row_mirror row_mask:0xf bank_mask:0xf
	s_waitcnt lgkmcnt(0)
	v_add_f32_e32 v34, v34, v35
	v_mov_b32_e32 v35, v34
	s_nop 1
	v_permlane16_swap_b32_e32 v34, v35
	s_waitcnt lgkmcnt(0)
	v_add_f32_e32 v34, v34, v35
	v_mov_b32_e32 v35, v34
	s_nop 1
	v_permlane32_swap_b32_e32 v34, v35
	s_cbranch_scc1 .LBB0_921
	s_add_i32 s28, s14, s13
	s_mul_hi_i32 s29, s28, 0x6000
	s_mulk_i32 s28, 0x6000
	s_add_u32 s28, s60, s28
	s_addc_u32 s29, s63, s29
	v_lshl_add_u64 v[16:17], v[56:57], 2, s[28:29]
	v_add_co_u32_e32 v8, vcc, 0x4000, v16
	s_mov_b64 s[28:29], 0x4000
	s_nop 0
	v_addc_co_u32_e32 v9, vcc, 0, v17, vcc
	global_load_dwordx4 v[4:7], v[60:61], off offset:16
	global_load_dwordx4 v[0:3], v[60:61], off
	v_lshl_add_u64 v[28:29], v[16:17], 0, s[28:29]
	global_load_dwordx4 v[8:11], v[8:9], off
	s_nop 0
	global_load_dwordx4 v[12:15], v[28:29], off offset:16
	s_mov_b64 s[28:29], 0x3000
	v_lshl_add_u64 v[40:41], v[16:17], 0, s[28:29]
	s_movk_i32 s28, 0x3000
	s_waitcnt vmcnt(1)
	v_pk_add_f32 v[8:9], v[8:9], 1.0 op_sel_hi:[1,0]
	s_nop 0
	v_pk_mul_f32 v[0:1], v[0:1], v[8:9]
	s_waitcnt vmcnt(0)
	v_pk_add_f32 v[8:9], v[14:15], 1.0 op_sel_hi:[1,0]
	v_pk_add_f32 v[10:11], v[10:11], 1.0 op_sel_hi:[1,0]
	v_pk_mul_f32 v[6:7], v[6:7], v[8:9]
	v_add_co_u32_e32 v8, vcc, s28, v16
	v_pk_mul_f32 v[2:3], v[2:3], v[10:11]
	v_pk_add_f32 v[10:11], v[12:13], 1.0 op_sel_hi:[1,0]
	v_addc_co_u32_e32 v9, vcc, 0, v17, vcc
	v_pk_mul_f32 v[4:5], v[4:5], v[10:11]
	global_load_dwordx4 v[8:11], v[8:9], off
	s_nop 0
	global_load_dwordx4 v[12:15], v[40:41], off offset:16
	global_load_dwordx4 v[20:23], v[60:61], off offset:2064
	global_load_dwordx4 v[16:19], v[60:61], off offset:2048
	global_load_dwordx4 v[24:27], v[28:29], off offset:2064
	s_nop 0
	global_load_dwordx4 v[28:31], v[28:29], off offset:2048
	s_waitcnt vmcnt(1)
	v_pk_add_f32 v[26:27], v[26:27], 1.0 op_sel_hi:[1,0]
	s_waitcnt vmcnt(0)
	v_pk_add_f32 v[30:31], v[30:31], 1.0 op_sel_hi:[1,0]
	v_pk_add_f32 v[28:29], v[28:29], 1.0 op_sel_hi:[1,0]
	v_pk_add_f32 v[24:25], v[24:25], 1.0 op_sel_hi:[1,0]
	v_pk_mul_f32 v[18:19], v[18:19], v[30:31]
	v_pk_mul_f32 v[16:17], v[16:17], v[28:29]
	v_pk_mul_f32 v[22:23], v[22:23], v[26:27]
	v_pk_mul_f32 v[20:21], v[20:21], v[24:25]
	global_load_dwordx4 v[24:27], v[40:41], off offset:2064
	global_load_dwordx4 v[28:31], v[40:41], off offset:2048
	s_branch .LBB0_921
